# v026-scalar-addressing-fmamix-movb64
# speedup vs baseline: 1.0936x; 1.0117x over previous
.LBB3_8:
	s_or_b64 exec, exec, s[2:3]
	s_movk_i32 s15, 0x61a8
	v_cmp_gt_i32_e32 vcc, s15, v56
	s_waitcnt lgkmcnt(0)
	s_barrier
	s_and_saveexec_b64 s[2:3], vcc
	s_cbranch_execz .LBB3_73
	s_load_dwordx4 s[16:19], s[0:1], 0x30
	v_and_b32_e32 v1, 63, v0
	s_waitcnt vmcnt(3)
	v_mov_b32_e32 v2, 0x3e020821
	v_cmp_gt_u32_e64 s[0:1], 32, v1
	v_mov_b32_e32 v65, 0xffff
	v_cmp_ne_u32_e32 vcc, 0, v52
	v_cndmask_b32_e64 v64, v2, 0, s[0:1]
	s_waitcnt vmcnt(0)
	v_lshrrev_b32_e32 v2, 16, v53
	v_lshrrev_b32_e32 v0, 1, v0
	v_mov_b32_e32 v3, 0x7a00
	v_ashrrev_i32_e32 v57, 31, v56
	v_cndmask_b32_e32 v77, v65, v2, vcc
	s_lshl_b32 s6, s6, 2
	v_lshlrev_b32_e32 v2, 4, v1
	v_and_or_b32 v67, v0, 16, v3
	v_lshlrev_b32_e32 v70, 1, v1
	v_lshlrev_b32_e32 v36, 2, v1
	v_lshlrev_b64 v[0:1], 8, v[56:57]
	v_mov_b32_e32 v37, 0
	v_or_b32_e32 v0, v0, v36
	s_ashr_i32 s7, s6, 31
	s_mov_b32 s5, 0
	v_add_u32_e32 v66, 0x3200, v2
	v_add_u32_e32 v68, 0x5200, v2
	v_add_u32_e32 v69, 0x7200, v2
	s_waitcnt lgkmcnt(0)
	v_lshl_add_u64 v[58:59], s[16:17], 0, v[36:37]
	s_mov_b64 s[60:61], s[16:17]
	v_lshl_add_u64 v[60:61], s[18:19], 0, v[0:1]
	s_lshl_b64 s[10:11], s[6:7], 8
	s_mov_b64 s[12:13], 0
	s_movk_i32 s7, 0x61a7
	v_mov_b32_e32 v57, 0xc0669d92
	s_mov_b32 s20, 0xc1c00000
	v_mov_b32_e32 v71, 0x41c00000
	v_mov_b32_e32 v72, 0xbfb8aa3b
	v_mov_b32_e32 v73, 0xc1b69213
	v_mov_b32_e32 v74, 0xc228283a
	v_mov_b32_e32 v75, 0xc275076b
	s_mov_b32 s14, 0x3e0a9555
	v_readfirstlane_b32 s94, v56
	s_nop 3
	v_lshlrev_b32_e32 v94, 4, v62
	s_lshl_b32 s95, s94, 8
	s_add_u32 s62, s18, s95
	s_addc_u32 s63, s19, 0
	v_lshlrev_b32_e32 v95, 1, v70
	s_branch .LBB3_11
.LBB3_10:
	s_and_b64 s[2:3], exec, s[2:3]
	s_or_b64 s[12:13], s[2:3], s[12:13]
	v_readlane_b32 s2, v34, 31
	s_bfe_u32 s3, s2, 0x80008
	v_lshl_or_b32 v2, s3, 7, v70
	ds_read_u16 v2, v2
	s_bfe_u32 s2, s2, 0x100010
	v_add_f32_e32 v1, v1, v15
	s_waitcnt lgkmcnt(1)
	v_fma_mix_f32 v0, v15, v35, v0 op_sel_hi:[0,1,0]
	s_lshl_b32 s4, s2, 8
	s_waitcnt lgkmcnt(0)
	v_fma_mix_f32 v2, v2, v1, v0 op_sel_hi:[1,0,0]
	s_add_u32 s58, s60, s4
	s_addc_u32 s59, s61, 0
	s_cmp_lg_u64 s[18:19], 0
	s_cselect_b32 s58, s58, s62
	s_cselect_b32 s59, s59, s63
	s_nop 0
	v_cndmask_b32_sdwa v77, v76, v65, vcc dst_sel:DWORD dst_unused:UNUSED_PAD src0_sel:WORD_1 src1_sel:DWORD
	s_nop 0
	s_nop 0
	s_add_u32 s62, s62, 0x100000
	s_addc_u32 s63, s63, 0
	v_mov_b64_e32 v[32:33], v[40:41]
	v_mov_b64_e32 v[34:35], v[42:43]
	global_store_dword v95, v2, s[58:59] sc1
	s_andn2_b64 exec, exec, s[12:13]
	s_cbranch_execz .LBB3_73

.Lprio_e0_done:
	s_mov_b32 s93, s94
	s_add_u32 s94, s94, 0x1000
	s_cmp_lt_u32 s94, 0x61a8
	s_cselect_b32 s95, s94, s93
	s_lshl_b32 s95, s95, 9
	s_add_u32 s56, s8, s95
	s_addc_u32 s57, s9, 0
	v_sub_f32_e32 v36, v32, v64
	v_fmamk_f32 v38, v36, 0x4297576a, v57
	v_fmamk_f32 v39, v36, 0x4297576a, v73
	v_med3_f32 v41, v38, s20, v71
	v_med3_f32 v43, v39, s20, v71
	v_mul_f32_e64 v38, v41, -v41
	v_mul_f32_e64 v39, v43, -v43
	v_exp_f32_e32 v38, v38
	v_exp_f32_e32 v39, v39
	v_fmamk_f32 v40, v41, 0x4019be61, v72
	v_fmamk_f32 v41, v41, 0xc019be61, v72
	v_exp_f32_e32 v42, v41
	v_pk_mul_f32 v[46:47], v[32:33], v[38:39] op_sel:[1,0]
	v_fmamk_f32 v38, v43, 0x4019be61, v72
	v_exp_f32_e32 v41, v38
	v_fmamk_f32 v38, v43, 0xc019be61, v72
	v_exp_f32_e32 v43, v38
	v_fmamk_f32 v38, v36, 0x4297576a, v74
	v_fmamk_f32 v36, v36, 0x4297576a, v75
	v_med3_f32 v45, v38, s20, v71
	v_med3_f32 v36, v36, s20, v71
	v_mul_f32_e64 v38, v45, -v45
	v_mul_f32_e64 v39, v36, -v36
	v_exp_f32_e32 v38, v38
	v_exp_f32_e32 v39, v39
	v_exp_f32_e32 v40, v40
	v_fmamk_f32 v44, v45, 0x4019be61, v72
	v_fmamk_f32 v45, v45, 0xc019be61, v72
	v_pk_mul_f32 v[54:55], v[32:33], v[38:39] op_sel:[1,0]
	v_fmamk_f32 v38, v36, 0x4019be61, v72
	v_exp_f32_e32 v48, v45
	v_exp_f32_e32 v45, v38
	v_pk_mul_f32 v[50:51], v[40:41], v[46:47]
	v_pk_mul_f32 v[38:39], v[40:41], s[14:15] op_sel_hi:[1,0]
	v_exp_f32_e32 v44, v44
	v_pk_mul_f32 v[52:53], v[38:39], v[50:51]
	v_pk_mul_f32 v[38:39], v[38:39], s[14:15] op_sel_hi:[1,0]
	ds_read_b128 v[12:15], v66
	ds_read_b128 v[8:11], v66 offset:1024
	ds_read_b128 v[4:7], v66 offset:2048
	ds_read_b128 v[0:3], v66 offset:3072
	ds_read_b128 v[16:19], v67
	ds_read_b128 v[20:23], v67 offset:32
	ds_read_b128 v[24:27], v67 offset:64
	ds_read_b128 v[28:31], v67 offset:96
	v_pk_mul_f32 v[78:79], v[38:39], v[52:53]
	v_pk_mul_f32 v[38:39], v[38:39], s[14:15] op_sel_hi:[1,0]
	v_pk_mul_f32 v[82:83], v[42:43], v[46:47]
	v_pk_mul_f32 v[80:81], v[38:39], v[78:79]
	v_pk_mul_f32 v[38:39], v[42:43], s[14:15] op_sel_hi:[1,0]
	v_pk_mul_f32 v[86:87], v[44:45], v[54:55]
	v_pk_mul_f32 v[42:43], v[38:39], v[82:83]
	v_pk_mul_f32 v[38:39], v[38:39], s[14:15] op_sel_hi:[1,0]
	v_cvt_pk_f16_f32 v40, v50, v52
	v_pk_mul_f32 v[84:85], v[38:39], v[42:43]
	v_pk_mul_f32 v[38:39], v[44:45], s[14:15] op_sel_hi:[1,0]
	v_cvt_pk_f16_f32 v41, v78, v80
	v_pk_mul_f32 v[88:89], v[38:39], v[86:87]
	v_pk_mul_f32 v[38:39], v[38:39], s[14:15] op_sel_hi:[1,0]
	v_fmamk_f32 v36, v36, 0xc019be61, v72
	v_pk_mul_f32 v[90:91], v[38:39], v[88:89]
	v_pk_mul_f32 v[44:45], v[38:39], s[14:15] op_sel_hi:[1,0]
	v_cvt_pk_f16_f32 v38, v84, v42
	v_cvt_pk_f16_f32 v39, v82, v46
	v_cvt_pk_f16_f32 v42, v85, v43
	v_cvt_pk_f16_f32 v43, v83, v47
	s_waitcnt lgkmcnt(0)
	v_mfma_f32_32x32x16_f16 v[16:31], v[12:15], v[38:41], v[16:31]
	v_mul_f32_e64 v12, v44, v90
	v_mul_f32_e64 v13, v45, v91
	v_cvt_pk_f16_f32 v44, v51, v53
	v_cvt_pk_f16_f32 v45, v79, v81
	v_exp_f32_e32 v49, v36
	ds_read_b128 v[50:53], v66 offset:4096
	v_cvt_pk_f16_f32 v82, v87, v89
	v_cvt_pk_f16_f32 v83, v91, v13
	v_mfma_f32_32x32x16_f16 v[16:31], v[8:11], v[42:45], v[16:31]
	v_mul_f32_e64 v14, v48, v54
	v_mul_f32_e64 v15, v49, v55
	v_mul_f32_e64 v48, v48, s14
	v_mul_f32_e64 v49, v49, s14
	v_cvt_pk_f16_f32 v47, v14, v54
	v_pk_mul_f32 v[8:9], v[48:49], v[14:15]
	v_pk_mul_f32 v[10:11], v[48:49], s[14:15] op_sel_hi:[1,0]
	v_cvt_pk_f16_f32 v48, v86, v88
	v_pk_mul_f32 v[10:11], v[10:11], v[8:9]
	v_cvt_pk_f16_f32 v49, v90, v12
	v_cvt_pk_f16_f32 v46, v10, v8
	v_cvt_pk_f16_f32 v80, v11, v9
	v_cvt_pk_f16_f32 v81, v15, v55
	v_mfma_f32_32x32x16_f16 v[16:31], v[4:7], v[46:49], v[16:31]
	s_nop 0
	v_add_u32_e32 v56, s6, v56
	s_nop 0
	v_mov_b32_e32 v78, v63
	v_readlane_b32 s21, v35, 0
	s_nop 0
	v_cmp_ne_u32_sdwa s[16:17], v78, v34 src0_sel:WORD_1 src1_sel:WORD_1
	v_mfma_f32_32x32x16_f16 v[16:31], v[0:3], v[80:83], v[16:31]
	ds_read_b128 v[0:3], v67 offset:128
	ds_read_b128 v[4:7], v67 offset:160
	ds_read_b128 v[8:11], v67 offset:192
	ds_read_b128 v[12:15], v67 offset:224
	ds_read_b128 v[84:87], v66 offset:5120
	s_nop 0
	s_nop 0
	s_nop 0
	s_nop 0
	s_nop 0
	s_nop 0
	s_waitcnt lgkmcnt(1)
	v_mfma_f32_32x32x16_f16 v[0:15], v[50:53], v[38:41], v[0:15]
	ds_read_b128 v[38:41], v66 offset:6144
	ds_read_b128 v[50:53], v66 offset:7168
	s_nop 0
	s_nop 0
	s_nop 2
	v_exp_f32_e32 v16, v16
	v_exp_f32_e32 v17, v17
	v_exp_f32_e32 v18, v18
	s_waitcnt lgkmcnt(2)
	v_mfma_f32_32x32x16_f16 v[0:15], v[84:87], v[42:45], v[0:15]
	v_exp_f32_e32 v19, v19
	v_exp_f32_e32 v20, v20
	v_exp_f32_e32 v21, v21
	v_exp_f32_e32 v22, v22
	v_exp_f32_e32 v23, v23
	v_pk_add_f32 v[16:17], v[16:17], 1.0 op_sel_hi:[1,0]
	v_pk_add_f32 v[18:19], v[18:19], 1.0 op_sel_hi:[1,0]
	s_waitcnt lgkmcnt(1)
	v_mfma_f32_32x32x16_f16 v[0:15], v[38:41], v[46:49], v[0:15]
	v_add_f32_e64 v20, v20, 1.0
	v_add_f32_e64 v21, v21, 1.0
	v_add_f32_e64 v22, v22, 1.0
	v_add_f32_e64 v23, v23, 1.0
	v_log_f32_e32 v16, v16
	v_log_f32_e32 v17, v17
	v_log_f32_e32 v18, v18
	v_log_f32_e32 v19, v19
	v_log_f32_e32 v20, v20
	s_waitcnt lgkmcnt(0)
	v_mfma_f32_32x32x16_f16 v[0:15], v[50:53], v[80:83], v[0:15]
	s_nop 0
	s_nop 0
	s_nop 0
	s_nop 0
	s_nop 0
	s_nop 0
	s_nop 11
	v_exp_f32_e32 v6, v6
	v_exp_f32_e32 v7, v7
	v_exp_f32_e32 v0, v0
	v_exp_f32_e32 v1, v1
	v_log_f32_e32 v21, v21
	v_pk_add_f32 v[6:7], v[6:7], 1.0 op_sel_hi:[1,0]
	v_log_f32_e32 v22, v22
	v_log_f32_e32 v6, v6
	v_log_f32_e32 v7, v7
	v_log_f32_e32 v23, v23
	s_nop 0
	s_nop 0
	v_exp_f32_e32 v4, v4
	v_exp_f32_e32 v5, v5
	s_nop 0
	v_exp_f32_e32 v2, v2
	v_exp_f32_e32 v3, v3
	s_mov_b64 vcc, 0
	v_pk_add_f32 v[0:1], v[0:1], 1.0 op_sel_hi:[1,0]
	v_pk_mul_f32 v[6:7], v[32:33], v[6:7] op_sel:[1,0]
	s_nop 0
	s_nop 0
	v_log_f32_e32 v0, v0
	v_log_f32_e32 v1, v1
	v_cvt_pk_f16_f32 v55, v6, v7
	s_nop 0
	s_nop 0
	s_nop 0
	s_nop 0
	v_pk_mul_f32 v[16:17], v[32:33], v[16:17] op_sel:[1,0]
	v_pk_mul_f32 v[18:19], v[32:33], v[18:19] op_sel:[1,0]
	v_pk_mul_f32 v[20:21], v[32:33], v[20:21] op_sel:[1,0]
	v_pk_mul_f32 v[22:23], v[32:33], v[22:23] op_sel:[1,0]
	v_pk_add_f32 v[4:5], v[4:5], 1.0 op_sel_hi:[1,0]
	v_exp_f32_e32 v6, v10
	v_exp_f32_e32 v7, v11
	s_nop 0
	global_load_dwordx4 v[40:43], v94, s[56:57]
	global_load_dword v63, v94, s[56:57] offset:24
	global_load_dword v76, v94, s[56:57] offset:-8
	v_cvt_pk_f16_f32 v47, v22, v23
	v_cvt_pk_f16_f32 v46, v20, v21
	v_cvt_pk_f16_f32 v45, v18, v19
	v_cvt_pk_f16_f32 v44, v16, v17
	s_nop 0
	s_nop 0
	s_nop 0
	s_nop 0
	s_nop 0
	s_nop 0
	s_nop 0
	s_nop 0
	v_pk_add_f32 v[2:3], v[2:3], 1.0 op_sel_hi:[1,0]
	v_log_f32_e32 v4, v4
	v_log_f32_e32 v5, v5
	s_nop 0
	s_nop 0
	v_exp_f32_e32 v16, v24
	v_exp_f32_e32 v17, v25
	v_exp_f32_e32 v18, v26
	v_exp_f32_e32 v19, v27
	v_exp_f32_e32 v20, v28
	v_exp_f32_e32 v21, v29
	v_exp_f32_e32 v22, v30
	v_exp_f32_e32 v23, v31
	v_log_f32_e32 v2, v2
	v_log_f32_e32 v3, v3
	v_exp_f32_e32 v8, v8
	v_exp_f32_e32 v9, v9
	v_pk_mul_f32 v[0:1], v[32:33], v[0:1] op_sel:[1,0]
	v_pk_mul_f32 v[4:5], v[32:33], v[4:5] op_sel:[1,0]
	v_cvt_pk_f16_f32 v52, v0, v1
	v_pk_add_f32 v[0:1], v[6:7], 1.0 op_sel_hi:[1,0]
	v_pk_add_f32 v[16:17], v[16:17], 1.0 op_sel_hi:[1,0]
	v_log_f32_e32 v10, v0
	s_nop 0
	v_pk_add_f32 v[18:19], v[18:19], 1.0 op_sel_hi:[1,0]
	v_pk_add_f32 v[20:21], v[20:21], 1.0 op_sel_hi:[1,0]
	v_pk_add_f32 v[22:23], v[22:23], 1.0 op_sel_hi:[1,0]
	v_pk_mul_f32 v[2:3], v[32:33], v[2:3] op_sel:[1,0]
	v_cvt_pk_f16_f32 v54, v4, v5
	v_pk_add_f32 v[4:5], v[8:9], 1.0 op_sel_hi:[1,0]
	v_exp_f32_e32 v12, v12
	s_nop 0
	v_log_f32_e32 v16, v16
	v_log_f32_e32 v17, v17
	v_log_f32_e32 v18, v18
	v_log_f32_e32 v19, v19
	v_log_f32_e32 v20, v20
	v_log_f32_e32 v21, v21
	v_log_f32_e32 v22, v22
	v_log_f32_e32 v23, v23
	v_log_f32_e32 v4, v4
	v_log_f32_e32 v5, v5
	v_cvt_pk_f16_f32 v53, v2, v3
	v_log_f32_e32 v11, v1
	v_exp_f32_e32 v13, v13
	ds_read_b128 v[0:3], v68
	v_pk_mul_f32 v[16:17], v[32:33], v[16:17] op_sel:[1,0]
	v_pk_mul_f32 v[18:19], v[32:33], v[18:19] op_sel:[1,0]
	v_pk_mul_f32 v[20:21], v[32:33], v[20:21] op_sel:[1,0]
	v_pk_mul_f32 v[22:23], v[32:33], v[22:23] op_sel:[1,0]
	v_pk_mul_f32 v[8:9], v[32:33], v[4:5] op_sel:[1,0]
	s_nop 0
	v_cvt_pk_f16_f32 v51, v22, v23
	v_cvt_pk_f16_f32 v50, v20, v21
	v_cvt_pk_f16_f32 v49, v18, v19
	v_cvt_pk_f16_f32 v48, v16, v17
	v_exp_f32_e32 v14, v14
	ds_read_b128 v[4:7], v68 offset:1024
	s_waitcnt lgkmcnt(1)
	v_mfma_f32_32x32x16_f16 v[16:31], v[44:47], v[0:3], 0
	s_nop 0
	v_add_f32_e64 v0, v12, 1.0
	v_add_f32_e64 v1, v13, 1.0
	v_exp_f32_e32 v15, v15
	v_log_f32_e32 v0, v0
	v_log_f32_e32 v1, v1
	v_pk_mul_f32 v[10:11], v[32:33], v[10:11] op_sel:[1,0]
	v_pk_add_f32 v[2:3], v[14:15], 1.0 op_sel_hi:[1,0]
	s_waitcnt lgkmcnt(0)
	v_mfma_f32_32x32x16_f16 v[16:31], v[48:51], v[4:7], v[16:31]
	v_log_f32_e32 v12, v2
	v_log_f32_e32 v13, v3
	v_pk_mul_f32 v[4:5], v[32:33], v[0:1] op_sel:[1,0]
	ds_read_b128 v[0:3], v68 offset:2048
	v_cvt_pk_f16_f32 v82, v4, v5
	v_pk_mul_f32 v[6:7], v[32:33], v[12:13] op_sel:[1,0]
	v_cvt_pk_f16_f32 v81, v10, v11
	v_cvt_pk_f16_f32 v83, v6, v7
	ds_read_b128 v[4:7], v68 offset:3072
	s_waitcnt lgkmcnt(1)
	v_mfma_f32_32x32x16_f16 v[16:31], v[52:55], v[0:3], v[16:31]
	v_cvt_pk_f16_f32 v80, v8, v9
	v_cvt_f16_f32_e32 v0, v33
	v_mov_b32_e32 v38, v37
	v_mov_b32_e32 v39, v37
	ds_read_b128 v[84:87], v69 offset:1024
	v_cndmask_b32_e64 v0, 0, v0, s[0:1]
	v_pack_b32_f16 v36, v0, 0
	s_waitcnt lgkmcnt(1)
	v_mfma_f32_32x32x16_f16 v[16:31], v[80:83], v[4:7], v[16:31]
	ds_read_b128 v[0:3], v69
	ds_read_b128 v[88:91], v68 offset:5120
	s_ashr_i32 s17, s21, 9
	v_readlane_b32 s22, v35, 1
	s_and_b32 s17, s17, 0xffffff80
	v_or_b32_e32 v32, s17, v70
	s_ashr_i32 s17, s22, 9
	s_waitcnt lgkmcnt(1)
	v_mfma_f32_32x32x16_f16 v[16:31], v[36:39], v[0:3], v[16:31]
	ds_read_b128 v[0:3], v68 offset:4096
	v_readlane_b32 s23, v35, 2
	s_and_b32 s17, s17, 0xffffff80
	v_or_b32_e32 v33, s17, v70
	s_ashr_i32 s17, s23, 9
	v_readlane_b32 s24, v35, 3
	s_and_b32 s17, s17, 0xffffff80
	s_waitcnt lgkmcnt(0)
	v_mfma_f32_32x32x16_f16 v[0:15], v[44:47], v[0:3], 0
	ds_read_b128 v[44:47], v68 offset:6144
	v_readlane_b32 s25, v35, 4
	v_readlane_b32 s26, v35, 5
	v_readlane_b32 s27, v35, 6
	v_readlane_b32 s28, v35, 7
	v_readlane_b32 s29, v35, 8
	v_readlane_b32 s30, v35, 9
	v_mfma_f32_32x32x16_f16 v[0:15], v[48:51], v[88:91], v[0:15]
	ds_read_b128 v[48:51], v68 offset:7168
	v_readlane_b32 s31, v35, 10
	v_readlane_b32 s33, v35, 11
	v_readlane_b32 s34, v35, 12
	v_readlane_b32 s35, v35, 13
	v_readlane_b32 s36, v35, 14
	v_readlane_b32 s37, v35, 15
	s_waitcnt lgkmcnt(1)
	v_mfma_f32_32x32x16_f16 v[0:15], v[52:55], v[44:47], v[0:15]
	v_readlane_b32 s38, v35, 16
	v_readlane_b32 s39, v35, 17
	v_readlane_b32 s40, v35, 18
	v_readlane_b32 s41, v35, 19
	v_readlane_b32 s42, v35, 20
	v_readlane_b32 s43, v35, 21
	v_readlane_b32 s44, v35, 22
	s_waitcnt lgkmcnt(0)
	v_mfma_f32_32x32x16_f16 v[0:15], v[80:83], v[48:51], v[0:15]
	v_readlane_b32 s45, v35, 23
	v_readlane_b32 s46, v35, 24
	v_readlane_b32 s47, v35, 25
	v_readlane_b32 s48, v35, 26
	v_readlane_b32 s49, v35, 27
	v_readlane_b32 s50, v35, 28
	v_readlane_b32 s51, v35, 29
	v_readlane_b32 s52, v35, 30
	v_readlane_b32 s4, v35, 31
	v_or_b32_e32 v35, s17, v70
	s_ashr_i32 s17, s24, 9
	s_and_b32 s17, s17, 0xffffff80
	v_mfma_f32_32x32x16_f16 v[0:15], v[36:39], v[84:87], v[0:15]
	v_or_b32_e32 v36, s17, v70
	s_ashr_i32 s17, s25, 9
	s_and_b32 s17, s17, 0xffffff80
	v_or_b32_e32 v38, s17, v70
	s_ashr_i32 s17, s26, 9
	s_and_b32 s17, s17, 0xffffff80
	v_or_b32_e32 v39, s17, v70
	s_ashr_i32 s17, s27, 9
	s_and_b32 s17, s17, 0xffffff80
	v_or_b32_e32 v44, s17, v70
	s_ashr_i32 s17, s28, 9
	s_and_b32 s17, s17, 0xffffff80
	v_or_b32_e32 v45, s17, v70
	s_ashr_i32 s17, s29, 9
	s_and_b32 s17, s17, 0xffffff80
	ds_read_u16 v32, v32
	ds_read_u16 v91, v33
	ds_read_u16 v90, v35
	ds_read_u16 v89, v36
	ds_read_u16 v88, v38
	ds_read_u16 v87, v39
	ds_read_u16 v86, v44
	ds_read_u16 v85, v45
	v_or_b32_e32 v33, s17, v70
	s_ashr_i32 s17, s30, 9
	s_and_b32 s17, s17, 0xffffff80
	v_or_b32_e32 v35, s17, v70
	s_ashr_i32 s17, s31, 9
	s_and_b32 s17, s17, 0xffffff80
	v_or_b32_e32 v36, s17, v70
	s_ashr_i32 s17, s33, 9
	s_and_b32 s17, s17, 0xffffff80
	v_or_b32_e32 v38, s17, v70
	s_ashr_i32 s17, s34, 9
	s_and_b32 s17, s17, 0xffffff80
	v_or_b32_e32 v39, s17, v70
	s_ashr_i32 s17, s35, 9
	s_and_b32 s17, s17, 0xffffff80
	v_or_b32_e32 v44, s17, v70
	s_ashr_i32 s17, s36, 9
	s_and_b32 s17, s17, 0xffffff80
	v_or_b32_e32 v45, s17, v70
	s_ashr_i32 s17, s37, 9
	s_and_b32 s17, s17, 0xffffff80
	v_or_b32_e32 v46, s17, v70
	s_ashr_i32 s17, s38, 9
	s_and_b32 s17, s17, 0xffffff80
	v_cmp_ne_u32_sdwa s[18:19], v77, v34 src0_sel:DWORD src1_sel:WORD_1
	ds_read_u16 v84, v33
	ds_read_u16 v83, v35
	ds_read_u16 v82, v36
	ds_read_u16 v81, v38
	ds_read_u16 v80, v39
	ds_read_u16 v79, v44
	ds_read_u16 v78, v45
	ds_read_u16 v77, v46
	v_or_b32_e32 v33, s17, v70
	s_ashr_i32 s17, s39, 9
	s_and_b32 s17, s17, 0xffffff80
	v_or_b32_e32 v35, s17, v70
	s_ashr_i32 s17, s40, 9
	s_and_b32 s17, s17, 0xffffff80
	v_or_b32_e32 v36, s17, v70
	s_ashr_i32 s17, s41, 9
	s_and_b32 s17, s17, 0xffffff80
	v_or_b32_e32 v38, s17, v70
	s_ashr_i32 s17, s42, 9
	s_and_b32 s17, s17, 0xffffff80
	v_or_b32_e32 v39, s17, v70
	s_ashr_i32 s17, s43, 9
	s_and_b32 s17, s17, 0xffffff80
	v_or_b32_e32 v44, s17, v70
	s_ashr_i32 s17, s44, 9
	s_and_b32 s17, s17, 0xffffff80
	v_or_b32_e32 v45, s17, v70
	s_ashr_i32 s17, s45, 9
	s_and_b32 s17, s17, 0xffffff80
	v_or_b32_e32 v46, s17, v70
	s_ashr_i32 s17, s46, 9
	s_and_b32 s17, s17, 0xffffff80
	ds_read_u16 v55, v33
	ds_read_u16 v54, v35
	ds_read_u16 v53, v36
	ds_read_u16 v52, v38
	ds_read_u16 v51, v39
	ds_read_u16 v50, v44
	ds_read_u16 v49, v45
	ds_read_u16 v48, v46
	v_or_b32_e32 v33, s17, v70
	s_ashr_i32 s17, s47, 9
	s_and_b32 s17, s17, 0xffffff80
	v_or_b32_e32 v35, s17, v70
	s_ashr_i32 s17, s48, 9
	s_and_b32 s17, s17, 0xffffff80
	v_or_b32_e32 v36, s17, v70
	s_ashr_i32 s17, s49, 9
	s_and_b32 s17, s17, 0xffffff80
	v_or_b32_e32 v38, s17, v70
	s_ashr_i32 s17, s50, 9
	s_and_b32 s17, s17, 0xffffff80
	v_or_b32_e32 v39, s17, v70
	s_ashr_i32 s17, s51, 9
	s_and_b32 s17, s17, 0xffffff80
	v_or_b32_e32 v92, s17, v70
	s_ashr_i32 s17, s52, 9
	s_and_b32 s17, s17, 0xffffff80
	v_or_b32_e32 v93, s17, v70
	ds_read_u16 v47, v33
	ds_read_u16 v46, v35
	ds_read_u16 v45, v36
	ds_read_u16 v44, v38
	ds_read_u16 v39, v39
	ds_read_u16 v38, v92
	ds_read_u16 v36, v93
	s_ashr_i32 s4, s4, 9
	s_and_b32 s4, s4, 0xffffff80
	s_waitcnt lgkmcnt(14)
	v_cvt_f32_f16_e32 v32, v32
	v_or_b32_e32 v33, s4, v70
	ds_read_u16 v35, v33
	s_waitcnt vmcnt(0)
	v_permlane32_swap_b32_e32 v16, v0
	s_bitcmp1_b32 s18, 0
	v_mul_f32_e32 v32, v16, v32
	v_mov_b32_e32 v33, v16
	v_cmp_lt_i32_e64 s[2:3], s7, v56
	v_permlane32_swap_b32_e32 v17, v1
	v_permlane32_swap_b32_e32 v18, v2
	v_permlane32_swap_b32_e32 v19, v3
	v_permlane32_swap_b32_e32 v20, v4
	v_permlane32_swap_b32_e32 v21, v5
	v_permlane32_swap_b32_e32 v22, v6
	v_permlane32_swap_b32_e32 v23, v7
	v_permlane32_swap_b32_e32 v24, v8
	v_permlane32_swap_b32_e32 v25, v9
	v_permlane32_swap_b32_e32 v26, v10
	v_permlane32_swap_b32_e32 v27, v11
	v_permlane32_swap_b32_e32 v28, v12
	v_permlane32_swap_b32_e32 v29, v13
	v_permlane32_swap_b32_e32 v30, v14
	v_permlane32_swap_b32_e32 v31, v15
	s_cselect_b64 s[18:19], -1, 0
	s_bitcmp0_b32 s16, 0
	v_pk_add_f32 v[32:33], v[32:33], 0 op_sel_hi:[1,0]
	s_cbranch_scc1 .LBB3_13
	v_readlane_b32 s4, v34, 0
	s_bfe_u32 s17, s4, 0x80008
	v_lshl_or_b32 v16, s17, 7, v70
	ds_read_u16 v16, v16
	s_bfe_u32 s4, s4, 0x100010
	s_lshl_b32 s4, s4, 8
	s_add_u32 s58, s60, s4
	s_addc_u32 s59, s61, 0
	s_cmp_lg_u64 s[18:19], 0
	s_cselect_b32 s58, s58, s62
	s_cselect_b32 s59, s59, s63
	s_nop 0
	s_waitcnt lgkmcnt(0)
	v_fma_mix_f32 v16, v16, v33, v32 op_sel_hi:[1,0,0]
	v_mov_b64_e32 v[32:33], 0
	s_nop 0
	s_mov_b64 s[18:19], -1
	s_nop 0
	global_store_dword v95, v16, s[58:59] sc1
.LBB3_13:
	s_nop 0
	s_bitcmp0_b32 s16, 1
	v_fma_mix_f32 v16, v17, v91, 0 op_sel_hi:[0,1,0]
	v_pk_add_f32 v[16:17], v[16:17], v[32:33]
	s_cbranch_scc1 .LBB3_15
	v_readlane_b32 s4, v34, 1
	s_bfe_u32 s17, s4, 0x80008
	v_lshl_or_b32 v32, s17, 7, v70
	ds_read_u16 v91, v32
	s_bfe_u32 s4, s4, 0x100010
	s_lshl_b32 s4, s4, 8
	s_add_u32 s58, s60, s4
	s_addc_u32 s59, s61, 0
	s_cmp_lg_u64 s[18:19], 0
	s_cselect_b32 s58, s58, s62
	s_cselect_b32 s59, s59, s63
	s_nop 0
	s_waitcnt lgkmcnt(0)
	v_fma_mix_f32 v16, v91, v17, v16 op_sel_hi:[1,0,0]
	s_nop 0
	global_store_dword v95, v16, s[58:59] sc1
	v_mov_b64_e32 v[16:17], 0
	s_mov_b64 s[18:19], -1
	s_nop 0
.LBB3_15:
	s_nop 0
	v_mov_b32_e32 v33, v18
	s_bitcmp0_b32 s16, 2
	v_fma_mix_f32 v32, v18, v90, 0 op_sel_hi:[0,1,0]
	v_pk_add_f32 v[16:17], v[32:33], v[16:17]
	s_cbranch_scc1 .LBB3_17
	v_readlane_b32 s4, v34, 2
	s_bfe_u32 s17, s4, 0x80008
	v_lshl_or_b32 v18, s17, 7, v70
	ds_read_u16 v18, v18
	s_bfe_u32 s4, s4, 0x100010
	s_lshl_b32 s4, s4, 8
	s_add_u32 s58, s60, s4
	s_addc_u32 s59, s61, 0
	s_cmp_lg_u64 s[18:19], 0
	s_cselect_b32 s58, s58, s62
	s_cselect_b32 s59, s59, s63
	s_nop 0
	s_waitcnt lgkmcnt(0)
	v_fma_mix_f32 v16, v18, v17, v16 op_sel_hi:[1,0,0]
	s_nop 0
	global_store_dword v95, v16, s[58:59] sc1
	v_mov_b64_e32 v[16:17], 0
	s_mov_b64 s[18:19], -1
	s_nop 0
.LBB3_17:
	s_nop 0
	s_bitcmp0_b32 s16, 3
	v_fma_mix_f32 v18, v19, v89, 0 op_sel_hi:[0,1,0]
	v_pk_add_f32 v[16:17], v[18:19], v[16:17]
	s_cbranch_scc1 .LBB3_19
	v_readlane_b32 s4, v34, 3
	s_bfe_u32 s17, s4, 0x80008
	v_lshl_or_b32 v18, s17, 7, v70
	ds_read_u16 v32, v18
	s_bfe_u32 s4, s4, 0x100010
	s_lshl_b32 s4, s4, 8
	s_add_u32 s58, s60, s4
	s_addc_u32 s59, s61, 0
	s_cmp_lg_u64 s[18:19], 0
	s_cselect_b32 s58, s58, s62
	s_cselect_b32 s59, s59, s63
	s_nop 0
	s_waitcnt lgkmcnt(0)
	v_fma_mix_f32 v16, v32, v17, v16 op_sel_hi:[1,0,0]
	s_nop 0
	global_store_dword v95, v16, s[58:59] sc1
	v_mov_b64_e32 v[16:17], 0
	s_mov_b64 s[18:19], -1
	s_nop 0
.LBB3_19:
	s_nop 0
	v_mov_b32_e32 v19, v0
	s_bitcmp0_b32 s16, 4
	v_fma_mix_f32 v18, v0, v88, 0 op_sel_hi:[0,1,0]
	v_pk_add_f32 v[16:17], v[18:19], v[16:17]
	s_cbranch_scc1 .LBB3_21
	v_readlane_b32 s4, v34, 4
	s_bfe_u32 s17, s4, 0x80008
	v_lshl_or_b32 v0, s17, 7, v70
	ds_read_u16 v0, v0
	s_bfe_u32 s4, s4, 0x100010
	s_lshl_b32 s4, s4, 8
	s_add_u32 s58, s60, s4
	s_addc_u32 s59, s61, 0
	s_cmp_lg_u64 s[18:19], 0
	s_cselect_b32 s58, s58, s62
	s_cselect_b32 s59, s59, s63
	s_nop 0
	s_waitcnt lgkmcnt(0)
	v_fma_mix_f32 v0, v0, v17, v16 op_sel_hi:[1,0,0]
	v_mov_b64_e32 v[16:17], 0
	s_nop 0
	s_mov_b64 s[18:19], -1
	s_nop 0
	global_store_dword v95, v0, s[58:59] sc1
.LBB3_21:
	s_nop 0
	s_bitcmp0_b32 s16, 5
	v_fma_mix_f32 v0, v1, v87, 0 op_sel_hi:[0,1,0]
	v_pk_add_f32 v[0:1], v[0:1], v[16:17]
	s_cbranch_scc1 .LBB3_23
	v_readlane_b32 s4, v34, 5
	s_bfe_u32 s17, s4, 0x80008
	v_lshl_or_b32 v16, s17, 7, v70
	ds_read_u16 v18, v16
	s_bfe_u32 s4, s4, 0x100010
	s_lshl_b32 s4, s4, 8
	s_add_u32 s58, s60, s4
	s_addc_u32 s59, s61, 0
	s_cmp_lg_u64 s[18:19], 0
	s_cselect_b32 s58, s58, s62
	s_cselect_b32 s59, s59, s63
	s_nop 0
	s_waitcnt lgkmcnt(0)
	v_fma_mix_f32 v0, v18, v1, v0 op_sel_hi:[1,0,0]
	s_nop 0
	global_store_dword v95, v0, s[58:59] sc1
	v_mov_b64_e32 v[0:1], 0
	s_mov_b64 s[18:19], -1
	s_nop 0
.LBB3_23:
	s_nop 0
	v_mov_b32_e32 v17, v2
	s_bitcmp0_b32 s16, 6
	v_fma_mix_f32 v16, v2, v86, 0 op_sel_hi:[0,1,0]
	v_pk_add_f32 v[0:1], v[16:17], v[0:1]
	s_cbranch_scc1 .LBB3_25
	v_readlane_b32 s4, v34, 6
	s_bfe_u32 s17, s4, 0x80008
	v_lshl_or_b32 v2, s17, 7, v70
	ds_read_u16 v2, v2
	s_bfe_u32 s4, s4, 0x100010
	s_lshl_b32 s4, s4, 8
	s_add_u32 s58, s60, s4
	s_addc_u32 s59, s61, 0
	s_cmp_lg_u64 s[18:19], 0
	s_cselect_b32 s58, s58, s62
	s_cselect_b32 s59, s59, s63
	s_nop 0
	s_waitcnt lgkmcnt(0)
	v_fma_mix_f32 v0, v2, v1, v0 op_sel_hi:[1,0,0]
	s_nop 0
	global_store_dword v95, v0, s[58:59] sc1
	v_mov_b64_e32 v[0:1], 0
	s_mov_b64 s[18:19], -1
	s_nop 0
.LBB3_25:
	s_nop 0
	s_bitcmp0_b32 s16, 7
	v_fma_mix_f32 v2, v3, v85, 0 op_sel_hi:[0,1,0]
	v_pk_add_f32 v[0:1], v[2:3], v[0:1]
	s_cbranch_scc1 .LBB3_27
	v_readlane_b32 s4, v34, 7
	s_bfe_u32 s17, s4, 0x80008
	v_lshl_or_b32 v2, s17, 7, v70
	ds_read_u16 v16, v2
	s_bfe_u32 s4, s4, 0x100010
	s_lshl_b32 s4, s4, 8
	s_add_u32 s58, s60, s4
	s_addc_u32 s59, s61, 0
	s_cmp_lg_u64 s[18:19], 0
	s_cselect_b32 s58, s58, s62
	s_cselect_b32 s59, s59, s63
	s_nop 0
	s_waitcnt lgkmcnt(0)
	v_fma_mix_f32 v0, v16, v1, v0 op_sel_hi:[1,0,0]
	s_nop 0
	global_store_dword v95, v0, s[58:59] sc1
	v_mov_b64_e32 v[0:1], 0
	s_mov_b64 s[18:19], -1
	s_nop 0
.LBB3_27:
	s_nop 0
	v_mov_b32_e32 v3, v20
	s_bitcmp0_b32 s16, 8
	v_fma_mix_f32 v2, v20, v84, 0 op_sel_hi:[0,1,0]
	v_pk_add_f32 v[0:1], v[2:3], v[0:1]
	s_cbranch_scc1 .LBB3_29
	v_readlane_b32 s4, v34, 8
	s_bfe_u32 s17, s4, 0x80008
	v_lshl_or_b32 v2, s17, 7, v70
	ds_read_u16 v16, v2
	s_bfe_u32 s4, s4, 0x100010
	s_lshl_b32 s4, s4, 8
	s_add_u32 s58, s60, s4
	s_addc_u32 s59, s61, 0
	s_cmp_lg_u64 s[18:19], 0
	s_cselect_b32 s58, s58, s62
	s_cselect_b32 s59, s59, s63
	s_nop 0
	s_waitcnt lgkmcnt(0)
	v_fma_mix_f32 v0, v16, v1, v0 op_sel_hi:[1,0,0]
	s_nop 0
	global_store_dword v95, v0, s[58:59] sc1
	v_mov_b64_e32 v[0:1], 0
	s_mov_b64 s[18:19], -1
	s_nop 0
.LBB3_29:
	s_nop 0
	s_bitcmp0_b32 s16, 9
	v_fma_mix_f32 v20, v21, v83, 0 op_sel_hi:[0,1,0]
	v_pk_add_f32 v[0:1], v[20:21], v[0:1]
	s_cbranch_scc1 .LBB3_31
	v_readlane_b32 s4, v34, 9
	s_bfe_u32 s17, s4, 0x80008
	v_lshl_or_b32 v2, s17, 7, v70
	ds_read_u16 v16, v2
	s_bfe_u32 s4, s4, 0x100010
	s_lshl_b32 s4, s4, 8
	s_add_u32 s58, s60, s4
	s_addc_u32 s59, s61, 0
	s_cmp_lg_u64 s[18:19], 0
	s_cselect_b32 s58, s58, s62
	s_cselect_b32 s59, s59, s63
	s_nop 0
	s_waitcnt lgkmcnt(0)
	v_fma_mix_f32 v0, v16, v1, v0 op_sel_hi:[1,0,0]
	s_nop 0
	global_store_dword v95, v0, s[58:59] sc1
	v_mov_b64_e32 v[0:1], 0
	s_mov_b64 s[18:19], -1
	s_nop 0
.LBB3_31:
	s_nop 0
	v_mov_b32_e32 v3, v22
	s_bitcmp0_b32 s16, 10
	v_fma_mix_f32 v2, v22, v82, 0 op_sel_hi:[0,1,0]
	v_pk_add_f32 v[0:1], v[2:3], v[0:1]
	s_cbranch_scc1 .LBB3_33
	v_readlane_b32 s4, v34, 10
	s_bfe_u32 s17, s4, 0x80008
	v_lshl_or_b32 v2, s17, 7, v70
	ds_read_u16 v16, v2
	s_bfe_u32 s4, s4, 0x100010
	s_lshl_b32 s4, s4, 8
	s_add_u32 s58, s60, s4
	s_addc_u32 s59, s61, 0
	s_cmp_lg_u64 s[18:19], 0
	s_cselect_b32 s58, s58, s62
	s_cselect_b32 s59, s59, s63
	s_nop 0
	s_waitcnt lgkmcnt(0)
	v_fma_mix_f32 v0, v16, v1, v0 op_sel_hi:[1,0,0]
	s_nop 0
	global_store_dword v95, v0, s[58:59] sc1
	v_mov_b64_e32 v[0:1], 0
	s_mov_b64 s[18:19], -1
	s_nop 0
.LBB3_33:
	s_nop 0
	s_bitcmp0_b32 s16, 11
	v_fma_mix_f32 v22, v23, v81, 0 op_sel_hi:[0,1,0]
	v_pk_add_f32 v[0:1], v[22:23], v[0:1]
	s_cbranch_scc1 .LBB3_35
	v_readlane_b32 s4, v34, 11
	s_bfe_u32 s17, s4, 0x80008
	v_lshl_or_b32 v2, s17, 7, v70
	ds_read_u16 v16, v2
	s_bfe_u32 s4, s4, 0x100010
	s_lshl_b32 s4, s4, 8
	s_add_u32 s58, s60, s4
	s_addc_u32 s59, s61, 0
	s_cmp_lg_u64 s[18:19], 0
	s_cselect_b32 s58, s58, s62
	s_cselect_b32 s59, s59, s63
	s_nop 0
	s_waitcnt lgkmcnt(0)
	v_fma_mix_f32 v0, v16, v1, v0 op_sel_hi:[1,0,0]
	s_nop 0
	global_store_dword v95, v0, s[58:59] sc1
	v_mov_b64_e32 v[0:1], 0
	s_mov_b64 s[18:19], -1
	s_nop 0
.LBB3_35:
	s_nop 0
	v_mov_b32_e32 v3, v4
	s_bitcmp0_b32 s16, 12
	v_fma_mix_f32 v2, v4, v80, 0 op_sel_hi:[0,1,0]
	v_pk_add_f32 v[0:1], v[2:3], v[0:1]
	s_cbranch_scc1 .LBB3_37
	v_readlane_b32 s4, v34, 12
	s_bfe_u32 s17, s4, 0x80008
	v_lshl_or_b32 v2, s17, 7, v70
	ds_read_u16 v4, v2
	s_bfe_u32 s4, s4, 0x100010
	s_lshl_b32 s4, s4, 8
	s_add_u32 s58, s60, s4
	s_addc_u32 s59, s61, 0
	s_cmp_lg_u64 s[18:19], 0
	s_cselect_b32 s58, s58, s62
	s_cselect_b32 s59, s59, s63
	s_nop 0
	s_waitcnt lgkmcnt(0)
	v_fma_mix_f32 v0, v4, v1, v0 op_sel_hi:[1,0,0]
	s_nop 0
	global_store_dword v95, v0, s[58:59] sc1
	v_mov_b64_e32 v[0:1], 0
	s_mov_b64 s[18:19], -1
	s_nop 0
.LBB3_37:
	s_nop 0
	s_bitcmp0_b32 s16, 13
	v_fma_mix_f32 v4, v5, v79, 0 op_sel_hi:[0,1,0]
	v_pk_add_f32 v[0:1], v[4:5], v[0:1]
	s_cbranch_scc1 .LBB3_39
	v_readlane_b32 s4, v34, 13
	s_bfe_u32 s17, s4, 0x80008
	v_lshl_or_b32 v2, s17, 7, v70
	ds_read_u16 v4, v2
	s_bfe_u32 s4, s4, 0x100010
	s_lshl_b32 s4, s4, 8
	s_add_u32 s58, s60, s4
	s_addc_u32 s59, s61, 0
	s_cmp_lg_u64 s[18:19], 0
	s_cselect_b32 s58, s58, s62
	s_cselect_b32 s59, s59, s63
	s_nop 0
	s_waitcnt lgkmcnt(0)
	v_fma_mix_f32 v0, v4, v1, v0 op_sel_hi:[1,0,0]
	s_nop 0
	global_store_dword v95, v0, s[58:59] sc1
	v_mov_b64_e32 v[0:1], 0
	s_mov_b64 s[18:19], -1
	s_nop 0
.LBB3_39:
	s_nop 0
	v_mov_b32_e32 v3, v6
	s_bitcmp0_b32 s16, 14
	v_fma_mix_f32 v2, v6, v78, 0 op_sel_hi:[0,1,0]
	v_pk_add_f32 v[0:1], v[2:3], v[0:1]
	s_cbranch_scc1 .LBB3_41
	v_readlane_b32 s4, v34, 14
	s_bfe_u32 s17, s4, 0x80008
	v_lshl_or_b32 v2, s17, 7, v70
	ds_read_u16 v4, v2
	s_bfe_u32 s4, s4, 0x100010
	s_lshl_b32 s4, s4, 8
	s_add_u32 s58, s60, s4
	s_addc_u32 s59, s61, 0
	s_cmp_lg_u64 s[18:19], 0
	s_cselect_b32 s58, s58, s62
	s_cselect_b32 s59, s59, s63
	s_nop 0
	s_waitcnt lgkmcnt(0)
	v_fma_mix_f32 v0, v4, v1, v0 op_sel_hi:[1,0,0]
	s_nop 0
	global_store_dword v95, v0, s[58:59] sc1
	v_mov_b64_e32 v[0:1], 0
	s_mov_b64 s[18:19], -1
	s_nop 0
.LBB3_41:
	s_nop 0
	s_bitcmp0_b32 s16, 15
	v_fma_mix_f32 v6, v7, v77, 0 op_sel_hi:[0,1,0]
	v_pk_add_f32 v[0:1], v[6:7], v[0:1]
	s_cbranch_scc1 .LBB3_43
	v_readlane_b32 s4, v34, 15
	s_bfe_u32 s17, s4, 0x80008
	v_lshl_or_b32 v2, s17, 7, v70
	ds_read_u16 v4, v2
	s_bfe_u32 s4, s4, 0x100010
	s_lshl_b32 s4, s4, 8
	s_add_u32 s58, s60, s4
	s_addc_u32 s59, s61, 0
	s_cmp_lg_u64 s[18:19], 0
	s_cselect_b32 s58, s58, s62
	s_cselect_b32 s59, s59, s63
	s_nop 0
	s_waitcnt lgkmcnt(0)
	v_fma_mix_f32 v0, v4, v1, v0 op_sel_hi:[1,0,0]
	s_nop 0
	global_store_dword v95, v0, s[58:59] sc1
	v_mov_b64_e32 v[0:1], 0
	s_mov_b64 s[18:19], -1
	s_nop 0
.LBB3_43:
	s_nop 0
	v_mov_b32_e32 v3, v24
	s_bitcmp0_b32 s16, 16
	v_fma_mix_f32 v2, v24, v55, 0 op_sel_hi:[0,1,0]
	v_pk_add_f32 v[0:1], v[2:3], v[0:1]
	s_cbranch_scc1 .LBB3_45
	v_readlane_b32 s4, v34, 16
	s_bfe_u32 s17, s4, 0x80008
	v_lshl_or_b32 v2, s17, 7, v70
	ds_read_u16 v4, v2
	s_bfe_u32 s4, s4, 0x100010
	s_lshl_b32 s4, s4, 8
	s_add_u32 s58, s60, s4
	s_addc_u32 s59, s61, 0
	s_cmp_lg_u64 s[18:19], 0
	s_cselect_b32 s58, s58, s62
	s_cselect_b32 s59, s59, s63
	s_nop 0
	s_waitcnt lgkmcnt(0)
	v_fma_mix_f32 v0, v4, v1, v0 op_sel_hi:[1,0,0]
	s_nop 0
	global_store_dword v95, v0, s[58:59] sc1
	v_mov_b64_e32 v[0:1], 0
	s_mov_b64 s[18:19], -1
	s_nop 0
.LBB3_45:
	s_waitcnt lgkmcnt(14)
	s_nop 0
	s_bitcmp0_b32 s16, 17
	v_fma_mix_f32 v24, v25, v54, 0 op_sel_hi:[0,1,0]
	v_pk_add_f32 v[0:1], v[24:25], v[0:1]
	s_cbranch_scc1 .LBB3_47
	v_readlane_b32 s4, v34, 17
	s_bfe_u32 s17, s4, 0x80008
	v_lshl_or_b32 v2, s17, 7, v70
	ds_read_u16 v4, v2
	s_bfe_u32 s4, s4, 0x100010
	s_lshl_b32 s4, s4, 8
	s_add_u32 s58, s60, s4
	s_addc_u32 s59, s61, 0
	s_cmp_lg_u64 s[18:19], 0
	s_cselect_b32 s58, s58, s62
	s_cselect_b32 s59, s59, s63
	s_nop 0
	s_waitcnt lgkmcnt(0)
	v_fma_mix_f32 v0, v4, v1, v0 op_sel_hi:[1,0,0]
	s_nop 0
	global_store_dword v95, v0, s[58:59] sc1
	v_mov_b64_e32 v[0:1], 0
	s_mov_b64 s[18:19], -1
	s_nop 0
.LBB3_47:
	s_waitcnt lgkmcnt(13)
	s_nop 0
	v_mov_b32_e32 v3, v26
	s_bitcmp0_b32 s16, 18
	v_fma_mix_f32 v2, v26, v53, 0 op_sel_hi:[0,1,0]
	v_pk_add_f32 v[0:1], v[2:3], v[0:1]
	s_cbranch_scc1 .LBB3_49
	v_readlane_b32 s4, v34, 18
	s_bfe_u32 s17, s4, 0x80008
	v_lshl_or_b32 v2, s17, 7, v70
	ds_read_u16 v4, v2
	s_bfe_u32 s4, s4, 0x100010
	s_lshl_b32 s4, s4, 8
	s_add_u32 s58, s60, s4
	s_addc_u32 s59, s61, 0
	s_cmp_lg_u64 s[18:19], 0
	s_cselect_b32 s58, s58, s62
	s_cselect_b32 s59, s59, s63
	s_nop 0
	s_waitcnt lgkmcnt(0)
	v_fma_mix_f32 v0, v4, v1, v0 op_sel_hi:[1,0,0]
	s_nop 0
	global_store_dword v95, v0, s[58:59] sc1
	v_mov_b64_e32 v[0:1], 0
	s_mov_b64 s[18:19], -1
	s_nop 0
.LBB3_49:
	s_waitcnt lgkmcnt(12)
	s_nop 0
	s_bitcmp0_b32 s16, 19
	v_fma_mix_f32 v26, v27, v52, 0 op_sel_hi:[0,1,0]
	v_pk_add_f32 v[0:1], v[26:27], v[0:1]
	s_cbranch_scc1 .LBB3_51
	v_readlane_b32 s4, v34, 19
	s_bfe_u32 s17, s4, 0x80008
	v_lshl_or_b32 v2, s17, 7, v70
	ds_read_u16 v4, v2
	s_bfe_u32 s4, s4, 0x100010
	s_lshl_b32 s4, s4, 8
	s_add_u32 s58, s60, s4
	s_addc_u32 s59, s61, 0
	s_cmp_lg_u64 s[18:19], 0
	s_cselect_b32 s58, s58, s62
	s_cselect_b32 s59, s59, s63
	s_nop 0
	s_waitcnt lgkmcnt(0)
	v_fma_mix_f32 v0, v4, v1, v0 op_sel_hi:[1,0,0]
	s_nop 0
	global_store_dword v95, v0, s[58:59] sc1
	v_mov_b64_e32 v[0:1], 0
	s_mov_b64 s[18:19], -1
	s_nop 0
.LBB3_51:
	s_waitcnt lgkmcnt(11)
	s_nop 0
	v_mov_b32_e32 v3, v8
	s_bitcmp0_b32 s16, 20
	v_fma_mix_f32 v2, v8, v51, 0 op_sel_hi:[0,1,0]
	v_pk_add_f32 v[0:1], v[2:3], v[0:1]
	s_cbranch_scc1 .LBB3_53
	v_readlane_b32 s4, v34, 20
	s_bfe_u32 s17, s4, 0x80008
	v_lshl_or_b32 v2, s17, 7, v70
	ds_read_u16 v4, v2
	s_bfe_u32 s4, s4, 0x100010
	s_lshl_b32 s4, s4, 8
	s_add_u32 s58, s60, s4
	s_addc_u32 s59, s61, 0
	s_cmp_lg_u64 s[18:19], 0
	s_cselect_b32 s58, s58, s62
	s_cselect_b32 s59, s59, s63
	s_nop 0
	s_waitcnt lgkmcnt(0)
	v_fma_mix_f32 v0, v4, v1, v0 op_sel_hi:[1,0,0]
	s_nop 0
	global_store_dword v95, v0, s[58:59] sc1
	v_mov_b64_e32 v[0:1], 0
	s_mov_b64 s[18:19], -1
	s_nop 0
.LBB3_53:
	s_waitcnt lgkmcnt(10)
	s_nop 0
	s_bitcmp0_b32 s16, 21
	v_fma_mix_f32 v8, v9, v50, 0 op_sel_hi:[0,1,0]
	v_pk_add_f32 v[0:1], v[8:9], v[0:1]
	s_cbranch_scc1 .LBB3_55
	v_readlane_b32 s4, v34, 21
	s_bfe_u32 s17, s4, 0x80008
	v_lshl_or_b32 v2, s17, 7, v70
	ds_read_u16 v4, v2
	s_bfe_u32 s4, s4, 0x100010
	s_lshl_b32 s4, s4, 8
	s_add_u32 s58, s60, s4
	s_addc_u32 s59, s61, 0
	s_cmp_lg_u64 s[18:19], 0
	s_cselect_b32 s58, s58, s62
	s_cselect_b32 s59, s59, s63
	s_nop 0
	s_waitcnt lgkmcnt(0)
	v_fma_mix_f32 v0, v4, v1, v0 op_sel_hi:[1,0,0]
	s_nop 0
	global_store_dword v95, v0, s[58:59] sc1
	v_mov_b64_e32 v[0:1], 0
	s_mov_b64 s[18:19], -1
	s_nop 0
.LBB3_55:
	s_waitcnt lgkmcnt(9)
	s_nop 0
	v_mov_b32_e32 v3, v10
	s_bitcmp0_b32 s16, 22
	v_fma_mix_f32 v2, v10, v49, 0 op_sel_hi:[0,1,0]
	v_pk_add_f32 v[0:1], v[2:3], v[0:1]
	s_cbranch_scc1 .LBB3_57
	v_readlane_b32 s4, v34, 22
	s_bfe_u32 s17, s4, 0x80008
	v_lshl_or_b32 v2, s17, 7, v70
	ds_read_u16 v4, v2
	s_bfe_u32 s4, s4, 0x100010
	s_lshl_b32 s4, s4, 8
	s_add_u32 s58, s60, s4
	s_addc_u32 s59, s61, 0
	s_cmp_lg_u64 s[18:19], 0
	s_cselect_b32 s58, s58, s62
	s_cselect_b32 s59, s59, s63
	s_nop 0
	s_waitcnt lgkmcnt(0)
	v_fma_mix_f32 v0, v4, v1, v0 op_sel_hi:[1,0,0]
	s_nop 0
	global_store_dword v95, v0, s[58:59] sc1
	v_mov_b64_e32 v[0:1], 0
	s_mov_b64 s[18:19], -1
	s_nop 0
.LBB3_57:
	s_waitcnt lgkmcnt(8)
	s_nop 0
	s_bitcmp0_b32 s16, 23
	v_fma_mix_f32 v10, v11, v48, 0 op_sel_hi:[0,1,0]
	v_pk_add_f32 v[0:1], v[10:11], v[0:1]
	s_cbranch_scc1 .LBB3_59
	v_readlane_b32 s4, v34, 23
	s_bfe_u32 s17, s4, 0x80008
	v_lshl_or_b32 v2, s17, 7, v70
	ds_read_u16 v4, v2
	s_bfe_u32 s4, s4, 0x100010
	s_lshl_b32 s4, s4, 8
	s_add_u32 s58, s60, s4
	s_addc_u32 s59, s61, 0
	s_cmp_lg_u64 s[18:19], 0
	s_cselect_b32 s58, s58, s62
	s_cselect_b32 s59, s59, s63
	s_nop 0
	s_waitcnt lgkmcnt(0)
	v_fma_mix_f32 v0, v4, v1, v0 op_sel_hi:[1,0,0]
	s_nop 0
	global_store_dword v95, v0, s[58:59] sc1
	v_mov_b64_e32 v[0:1], 0
	s_mov_b64 s[18:19], -1
	s_nop 0
.LBB3_59:
	s_waitcnt lgkmcnt(7)
	s_nop 0
	v_mov_b32_e32 v3, v28
	s_bitcmp0_b32 s16, 24
	v_fma_mix_f32 v2, v28, v47, 0 op_sel_hi:[0,1,0]
	v_pk_add_f32 v[0:1], v[2:3], v[0:1]
	s_cbranch_scc1 .LBB3_61
	v_readlane_b32 s4, v34, 24
	s_bfe_u32 s17, s4, 0x80008
	v_lshl_or_b32 v2, s17, 7, v70
	ds_read_u16 v4, v2
	s_bfe_u32 s4, s4, 0x100010
	s_lshl_b32 s4, s4, 8
	s_add_u32 s58, s60, s4
	s_addc_u32 s59, s61, 0
	s_cmp_lg_u64 s[18:19], 0
	s_cselect_b32 s58, s58, s62
	s_cselect_b32 s59, s59, s63
	s_nop 0
	s_waitcnt lgkmcnt(0)
	v_fma_mix_f32 v0, v4, v1, v0 op_sel_hi:[1,0,0]
	s_nop 0
	global_store_dword v95, v0, s[58:59] sc1
	v_mov_b64_e32 v[0:1], 0
	s_mov_b64 s[18:19], -1
	s_nop 0
.LBB3_61:
	s_waitcnt lgkmcnt(6)
	s_nop 0
	s_bitcmp0_b32 s16, 25
	v_fma_mix_f32 v28, v29, v46, 0 op_sel_hi:[0,1,0]
	v_pk_add_f32 v[0:1], v[28:29], v[0:1]
	s_cbranch_scc1 .LBB3_63
	v_readlane_b32 s4, v34, 25
	s_bfe_u32 s17, s4, 0x80008
	v_lshl_or_b32 v2, s17, 7, v70
	ds_read_u16 v4, v2
	s_bfe_u32 s4, s4, 0x100010
	s_lshl_b32 s4, s4, 8
	s_add_u32 s58, s60, s4
	s_addc_u32 s59, s61, 0
	s_cmp_lg_u64 s[18:19], 0
	s_cselect_b32 s58, s58, s62
	s_cselect_b32 s59, s59, s63
	s_nop 0
	s_waitcnt lgkmcnt(0)
	v_fma_mix_f32 v0, v4, v1, v0 op_sel_hi:[1,0,0]
	s_nop 0
	global_store_dword v95, v0, s[58:59] sc1
	v_mov_b64_e32 v[0:1], 0
	s_mov_b64 s[18:19], -1
	s_nop 0
.LBB3_63:
	s_waitcnt lgkmcnt(5)
	s_nop 0
	v_mov_b32_e32 v3, v30
	s_bitcmp0_b32 s16, 26
	v_fma_mix_f32 v2, v30, v45, 0 op_sel_hi:[0,1,0]
	v_pk_add_f32 v[0:1], v[2:3], v[0:1]
	s_cbranch_scc1 .LBB3_65
	v_readlane_b32 s4, v34, 26
	s_bfe_u32 s17, s4, 0x80008
	v_lshl_or_b32 v2, s17, 7, v70
	ds_read_u16 v4, v2
	s_bfe_u32 s4, s4, 0x100010
	s_lshl_b32 s4, s4, 8
	s_add_u32 s58, s60, s4
	s_addc_u32 s59, s61, 0
	s_cmp_lg_u64 s[18:19], 0
	s_cselect_b32 s58, s58, s62
	s_cselect_b32 s59, s59, s63
	s_nop 0
	s_waitcnt lgkmcnt(0)
	v_fma_mix_f32 v0, v4, v1, v0 op_sel_hi:[1,0,0]
	s_nop 0
	global_store_dword v95, v0, s[58:59] sc1
	v_mov_b64_e32 v[0:1], 0
	s_mov_b64 s[18:19], -1
	s_nop 0
.LBB3_65:
	s_waitcnt lgkmcnt(4)
	s_nop 0
	s_bitcmp0_b32 s16, 27
	v_fma_mix_f32 v30, v31, v44, 0 op_sel_hi:[0,1,0]
	v_pk_add_f32 v[0:1], v[30:31], v[0:1]
	s_cbranch_scc1 .LBB3_67
	v_readlane_b32 s4, v34, 27
	s_bfe_u32 s17, s4, 0x80008
	v_lshl_or_b32 v2, s17, 7, v70
	ds_read_u16 v4, v2
	s_bfe_u32 s4, s4, 0x100010
	s_lshl_b32 s4, s4, 8
	s_add_u32 s58, s60, s4
	s_addc_u32 s59, s61, 0
	s_cmp_lg_u64 s[18:19], 0
	s_cselect_b32 s58, s58, s62
	s_cselect_b32 s59, s59, s63
	s_nop 0
	s_waitcnt lgkmcnt(0)
	v_fma_mix_f32 v0, v4, v1, v0 op_sel_hi:[1,0,0]
	s_nop 0
	global_store_dword v95, v0, s[58:59] sc1
	v_mov_b64_e32 v[0:1], 0
	s_mov_b64 s[18:19], -1
	s_nop 0
.LBB3_67:
	s_waitcnt lgkmcnt(3)
	s_nop 0
	v_mov_b32_e32 v3, v12
	s_bitcmp0_b32 s16, 28
	v_fma_mix_f32 v2, v12, v39, 0 op_sel_hi:[0,1,0]
	v_pk_add_f32 v[0:1], v[2:3], v[0:1]
	s_cbranch_scc1 .LBB3_69
	v_readlane_b32 s4, v34, 28
	s_bfe_u32 s17, s4, 0x80008
	v_lshl_or_b32 v2, s17, 7, v70
	ds_read_u16 v4, v2
	s_bfe_u32 s4, s4, 0x100010
	s_lshl_b32 s4, s4, 8
	s_add_u32 s58, s60, s4
	s_addc_u32 s59, s61, 0
	s_cmp_lg_u64 s[18:19], 0
	s_cselect_b32 s58, s58, s62
	s_cselect_b32 s59, s59, s63
	s_nop 0
	s_waitcnt lgkmcnt(0)
	v_fma_mix_f32 v0, v4, v1, v0 op_sel_hi:[1,0,0]
	s_nop 0
	global_store_dword v95, v0, s[58:59] sc1
	v_mov_b64_e32 v[0:1], 0
	s_mov_b64 s[18:19], -1
	s_nop 0
.LBB3_69:
	s_waitcnt lgkmcnt(2)
	s_nop 0
	s_bitcmp0_b32 s16, 29
	v_fma_mix_f32 v12, v13, v38, 0 op_sel_hi:[0,1,0]
	v_pk_add_f32 v[0:1], v[12:13], v[0:1]
	s_cbranch_scc1 .LBB3_71
	v_readlane_b32 s4, v34, 29
	s_bfe_u32 s17, s4, 0x80008
	v_lshl_or_b32 v2, s17, 7, v70
	ds_read_u16 v4, v2
	s_bfe_u32 s4, s4, 0x100010
	s_lshl_b32 s4, s4, 8
	s_add_u32 s58, s60, s4
	s_addc_u32 s59, s61, 0
	s_cmp_lg_u64 s[18:19], 0
	s_cselect_b32 s58, s58, s62
	s_cselect_b32 s59, s59, s63
	s_nop 0
	s_waitcnt lgkmcnt(0)
	v_fma_mix_f32 v0, v4, v1, v0 op_sel_hi:[1,0,0]
	s_nop 0
	global_store_dword v95, v0, s[58:59] sc1
	v_mov_b64_e32 v[0:1], 0
	s_mov_b64 s[18:19], -1
	s_nop 0
.LBB3_71:
	s_waitcnt lgkmcnt(1)
	s_nop 0
	v_mov_b32_e32 v3, v14
	s_bitcmp0_b32 s16, 30
	v_fma_mix_f32 v2, v14, v36, 0 op_sel_hi:[0,1,0]
	v_pk_add_f32 v[0:1], v[2:3], v[0:1]
	s_cbranch_scc1 .LBB3_10
	v_readlane_b32 s4, v34, 30
	s_bfe_u32 s16, s4, 0x80008
	v_lshl_or_b32 v2, s16, 7, v70
	ds_read_u16 v4, v2
	s_bfe_u32 s4, s4, 0x100010
	s_lshl_b32 s4, s4, 8
	s_add_u32 s58, s60, s4
	s_addc_u32 s59, s61, 0
	s_cmp_lg_u64 s[18:19], 0
	s_cselect_b32 s58, s58, s62
	s_cselect_b32 s59, s59, s63
	s_nop 0
	s_waitcnt lgkmcnt(0)
	v_fma_mix_f32 v0, v4, v1, v0 op_sel_hi:[1,0,0]
	s_nop 0
	global_store_dword v95, v0, s[58:59] sc1
	v_mov_b64_e32 v[0:1], 0
	s_mov_b64 s[18:19], -1
	s_nop 0
	s_branch .LBB3_10

	.amdhsa_kernel _Z7k_edge0PK15HIP_vector_typeIfLj4EEPKDv8_DF16_S5_PKfS7_S7_PfS8_
		.amdhsa_group_segment_fixed_size 31488
		.amdhsa_private_segment_fixed_size 0
		.amdhsa_kernarg_size 320
		.amdhsa_user_sgpr_count 2
		.amdhsa_user_sgpr_dispatch_ptr 0
		.amdhsa_user_sgpr_queue_ptr 0
		.amdhsa_user_sgpr_kernarg_segment_ptr 1
		.amdhsa_user_sgpr_dispatch_id 0
		.amdhsa_user_sgpr_kernarg_preload_length 0
		.amdhsa_user_sgpr_kernarg_preload_offset 0
		.amdhsa_user_sgpr_private_segment_size 0
		.amdhsa_uses_dynamic_stack 0
		.amdhsa_enable_private_segment 0
		.amdhsa_system_sgpr_workgroup_id_x 1
		.amdhsa_system_sgpr_workgroup_id_y 0
		.amdhsa_system_sgpr_workgroup_id_z 0
		.amdhsa_system_sgpr_workgroup_info 0
		.amdhsa_system_vgpr_workitem_id 0
		.amdhsa_next_free_vgpr 96
		.amdhsa_next_free_sgpr 96
		.amdhsa_accum_offset 96
		.amdhsa_reserve_vcc 1
		.amdhsa_float_round_mode_32 0
		.amdhsa_float_round_mode_16_64 0
		.amdhsa_float_denorm_mode_32 3
		.amdhsa_float_denorm_mode_16_64 3
		.amdhsa_dx10_clamp 1
		.amdhsa_ieee_mode 1
		.amdhsa_fp16_overflow 0
		.amdhsa_tg_split 0
		.amdhsa_exception_fp_ieee_invalid_op 0
		.amdhsa_exception_fp_denorm_src 0
		.amdhsa_exception_fp_ieee_div_zero 0
		.amdhsa_exception_fp_ieee_overflow 0
		.amdhsa_exception_fp_ieee_underflow 0
		.amdhsa_exception_fp_ieee_inexact 0
		.amdhsa_exception_int_div_zero 0
	.end_amdhsa_kernel

.LBB4_8:
	s_or_b64 exec, exec, s[2:3]
	s_movk_i32 s17, 0x61a8
	v_cmp_gt_i32_e32 vcc, s17, v64
	s_waitcnt lgkmcnt(0)
	s_barrier
	s_and_saveexec_b64 s[2:3], vcc
	s_cbranch_execz .LBB4_73
	s_load_dwordx4 s[4:7], s[0:1], 0x30
	s_load_dwordx2 s[2:3], s[0:1], 0x40
	v_and_b32_e32 v1, 63, v0
	s_waitcnt vmcnt(3)
	v_mov_b32_e32 v2, 0x3e020821
	v_cmp_gt_u32_e64 s[0:1], 32, v1
	v_mov_b32_e32 v68, 0xffff
	v_cmp_ne_u32_e32 vcc, 0, v54
	v_cndmask_b32_e64 v67, v2, 0, s[0:1]
	s_waitcnt vmcnt(0)
	v_lshrrev_b32_e32 v2, 16, v55
	v_lshrrev_b32_e32 v0, 1, v0
	v_mov_b32_e32 v3, 0x7a00
	v_ashrrev_i32_e32 v65, 31, v64
	v_lshlrev_b32_e32 v52, 2, v1
	v_cndmask_b32_e32 v95, v68, v2, vcc
	s_lshl_b32 s12, s10, 2
	v_lshlrev_b32_e32 v2, 4, v1
	v_and_or_b32 v70, v0, 16, v3
	v_lshlrev_b32_e32 v73, 1, v1
	v_lshlrev_b64 v[0:1], 8, v[64:65]
	v_mov_b32_e32 v53, 0
	v_or_b32_e32 v0, v0, v52
	s_ashr_i32 s13, s12, 31
	s_mov_b32 s11, 0
	v_add_u32_e32 v69, 0x3200, v2
	v_add_u32_e32 v71, 0x5200, v2
	v_add_u32_e32 v72, 0x7200, v2
	s_waitcnt lgkmcnt(0)
	v_lshl_add_u64 v[60:61], s[6:7], 0, v[52:53]
	s_mov_b64 s[60:61], s[6:7]
	v_lshl_add_u64 v[62:63], s[2:3], 0, v[0:1]
	s_lshl_b64 s[6:7], s[12:13], 8
	s_mov_b64 s[14:15], 0
	s_movk_i32 s13, 0x61a7
	v_mov_b32_e32 v65, 0xc0669d92
	s_mov_b32 s22, 0xc1c00000
	v_mov_b32_e32 v74, 0x41c00000
	v_mov_b32_e32 v75, 0xbfb8aa3b
	v_mov_b32_e32 v76, 0xc1b69213
	v_mov_b32_e32 v77, 0xc228283a
	v_mov_b32_e32 v78, 0xc275076b
	s_mov_b32 s16, 0x3e0a9555
	v_mov_b32_e32 v79, v52
	v_readfirstlane_b32 s94, v64
	s_nop 3
	v_lshlrev_b32_e32 v124, 4, v66
	s_lshl_b32 s95, s94, 8
	s_add_u32 s62, s2, s95
	s_addc_u32 s63, s3, 0
	s_branch .LBB4_11
.LBB4_10:
	s_and_b64 s[2:3], exec, s[2:3]
	s_or_b64 s[14:15], s[2:3], s[14:15]
	v_readlane_b32 s2, v50, 31
	s_bfe_u32 s3, s2, 0x80008
	v_lshl_or_b32 v0, s3, 7, v73
	ds_read_u16 v0, v0
	s_bfe_u32 s2, s2, 0x100010
	s_lshl_b32 s10, s2, 8
	v_fma_mix_f32 v32, v15, v81, v32 op_sel:[0,1,0] op_sel_hi:[0,1,0]
	v_fma_mix_f32 v33, v15, v81, v33 op_sel_hi:[0,1,0]
	s_nop 0
	v_cndmask_b32_sdwa v95, v51, v68, vcc dst_sel:DWORD dst_unused:UNUSED_PAD src0_sel:WORD_1 src1_sel:DWORD
	s_waitcnt lgkmcnt(0)
	v_fma_mix_f32 v2, v0, v33, v32 op_sel_hi:[1,0,0]
	s_add_u32 s58, s60, s10
	s_addc_u32 s59, s61, 0
	s_cmp_lg_u64 s[20:21], 0
	s_cselect_b32 s58, s58, s62
	s_cselect_b32 s59, s59, s63
	s_nop 0
	s_nop 0
	s_add_u32 s62, s62, 0x100000
	s_addc_u32 s63, s63, 0
	v_mov_b64_e32 v[48:49], v[56:57]
	v_mov_b64_e32 v[50:51], v[58:59]
	global_store_dword v79, v2, s[58:59] sc1
	s_andn2_b64 exec, exec, s[14:15]
	s_cbranch_execz .LBB4_73

.Lprio_e1_done:
	s_mov_b32 s93, s94
	s_add_u32 s94, s94, 0x1000
	s_cmp_lt_u32 s94, 0x61a8
	s_cselect_b32 s95, s94, s93
	s_lshl_b32 s95, s95, 9
	s_add_u32 s56, s8, s95
	s_addc_u32 s57, s9, 0
	v_sub_f32_e32 v39, v48, v67
	v_fmamk_f32 v32, v39, 0x4297576a, v65
	v_fmamk_f32 v33, v39, 0x4297576a, v76
	v_med3_f32 v35, v32, s22, v74
	v_med3_f32 v37, v33, s22, v74
	v_mul_f32_e64 v32, v35, -v35
	v_fmamk_f32 v34, v35, 0x4019be61, v75
	v_mul_f32_e64 v33, v37, -v37
	v_fmamk_f32 v35, v35, 0xc019be61, v75
	v_exp_f32_e32 v32, v32
	v_exp_f32_e32 v33, v33
	v_exp_f32_e32 v36, v35
	v_fmamk_f32 v35, v37, 0x4019be61, v75
	v_exp_f32_e32 v34, v34
	v_exp_f32_e32 v35, v35
	v_fmamk_f32 v37, v37, 0xc019be61, v75
	v_exp_f32_e32 v37, v37
	v_pk_mul_f32 v[32:33], v[48:49], v[32:33] op_sel:[1,0]
	ds_read_b128 v[28:31], v69
	ds_read_b128 v[24:27], v69 offset:1024
	ds_read_b128 v[20:23], v69 offset:2048
	ds_read_b128 v[16:19], v69 offset:3072
	ds_read_b128 v[0:3], v70
	ds_read_b128 v[4:7], v70 offset:32
	ds_read_b128 v[8:11], v70 offset:64
	ds_read_b128 v[12:15], v70 offset:96
	v_pk_mul_f32 v[44:45], v[34:35], v[32:33]
	v_pk_mul_f32 v[34:35], v[34:35], s[16:17] op_sel_hi:[1,0]
	v_mov_b32_e32 v99, v80
	v_fmamk_f32 v38, v39, 0x4297576a, v77
	v_fmamk_f32 v39, v39, 0x4297576a, v78
	v_pk_mul_f32 v[46:47], v[34:35], v[44:45]
	v_pk_mul_f32 v[34:35], v[34:35], s[16:17] op_sel_hi:[1,0]
	v_pk_mul_f32 v[80:81], v[36:37], v[32:33]
	v_pk_mul_f32 v[36:37], v[36:37], s[16:17] op_sel_hi:[1,0]
	v_med3_f32 v41, v38, s22, v74
	v_med3_f32 v43, v39, s22, v74
	v_pk_mul_f32 v[58:59], v[34:35], v[46:47]
	v_pk_mul_f32 v[34:35], v[34:35], s[16:17] op_sel_hi:[1,0]
	v_pk_mul_f32 v[82:83], v[36:37], v[80:81]
	v_pk_mul_f32 v[36:37], v[36:37], s[16:17] op_sel_hi:[1,0]
	v_mul_f32_e64 v38, v41, -v41
	v_fmamk_f32 v40, v41, 0x4019be61, v75
	v_mul_f32_e64 v39, v43, -v43
	v_fmamk_f32 v41, v41, 0xc019be61, v75
	v_pk_mul_f32 v[34:35], v[34:35], v[58:59]
	v_pk_mul_f32 v[36:37], v[36:37], v[82:83]
	v_exp_f32_e32 v38, v38
	v_exp_f32_e32 v39, v39
	v_exp_f32_e32 v42, v41
	v_fmamk_f32 v41, v43, 0x4019be61, v75
	v_cvt_pk_f16_f32 v56, v44, v46
	v_cvt_pk_f16_f32 v54, v36, v82
	v_cvt_pk_f16_f32 v57, v58, v34
	v_cvt_pk_f16_f32 v55, v80, v32
	v_exp_f32_e32 v40, v40
	v_exp_f32_e32 v41, v41
	s_waitcnt lgkmcnt(0)
	v_mfma_f32_32x32x16_f16 v[0:15], v[28:31], v[54:57], v[0:15]
	v_mul_f32_e64 v38, v49, v38
	v_mul_f32_e64 v39, v49, v39
	v_fmamk_f32 v43, v43, 0xc019be61, v75
	v_mul_f32_e64 v84, v40, v38
	v_mul_f32_e64 v85, v41, v39
	v_pk_mul_f32 v[40:41], v[40:41], s[16:17] op_sel_hi:[1,0]
	v_cvt_pk_f16_f32 v30, v45, v47
	v_pk_mul_f32 v[86:87], v[40:41], v[84:85]
	v_pk_mul_f32 v[28:29], v[40:41], s[16:17] op_sel_hi:[1,0]
	v_cvt_pk_f16_f32 v31, v59, v35
	v_pk_mul_f32 v[40:41], v[28:29], v[86:87]
	v_pk_mul_f32 v[28:29], v[28:29], s[16:17] op_sel_hi:[1,0]
	v_exp_f32_e32 v43, v43
	v_pk_mul_f32 v[88:89], v[28:29], v[40:41]
	v_cvt_pk_f16_f32 v28, v37, v83
	v_cvt_pk_f16_f32 v29, v81, v33
	v_pk_mul_f32 v[36:37], v[42:43], v[38:39]
	v_pk_mul_f32 v[42:43], v[42:43], s[16:17] op_sel_hi:[1,0]
	v_mfma_f32_32x32x16_f16 v[0:15], v[24:27], v[28:31], v[0:15]
	v_mul_f32_e64 v32, v42, v36
	v_mul_f32_e64 v33, v43, v37
	v_mul_f32_e64 v24, v42, s16
	v_mul_f32_e64 v25, v43, s16
	v_cvt_pk_f16_f32 v26, v84, v86
	v_pk_mul_f32 v[34:35], v[24:25], v[32:33]
	v_cvt_pk_f16_f32 v27, v40, v88
	v_cvt_pk_f16_f32 v24, v34, v32
	v_cvt_pk_f16_f32 v25, v36, v38
	v_cvt_pk_f16_f32 v84, v85, v87
	v_cvt_pk_f16_f32 v82, v35, v33
	v_mfma_f32_32x32x16_f16 v[0:15], v[20:23], v[24:27], v[0:15]
	ds_read_b128 v[20:23], v69 offset:4096
	v_cvt_pk_f16_f32 v85, v41, v89
	v_cvt_pk_f16_f32 v83, v37, v39
	ds_read_b128 v[32:35], v70 offset:128
	ds_read_b128 v[36:39], v70 offset:160
	ds_read_b128 v[40:43], v70 offset:192
	ds_read_b128 v[44:47], v70 offset:224
	s_nop 0
	v_add_u32_e32 v64, s12, v64
	v_readlane_b32 s48, v51, 0
	v_mfma_f32_32x32x16_f16 v[0:15], v[16:19], v[82:85], v[0:15]
	ds_read_b128 v[16:19], v69 offset:5120
	s_nop 0
	s_lshl_b32 s48, s48, 8
	s_and_b32 s48, s48, 0xffff00
	v_readlane_b32 s47, v51, 1
	s_add_u32 s48, s4, s48
	s_addc_u32 s49, s5, 0
	s_waitcnt lgkmcnt(1)
	v_mfma_f32_32x32x16_f16 v[32:47], v[20:23], v[54:57], v[32:47]
	ds_read_b128 v[20:23], v69 offset:6144
	s_lshl_b32 s47, s47, 8
	s_and_b32 s47, s47, 0xffff00
	v_readlane_b32 s46, v51, 2
	v_readlane_b32 s45, v51, 3
	v_readlane_b32 s44, v51, 4
	v_readlane_b32 s43, v51, 5
	s_waitcnt lgkmcnt(1)
	v_mfma_f32_32x32x16_f16 v[32:47], v[16:19], v[28:31], v[32:47]
	s_nop 0
	s_nop 0
	s_mov_b64 vcc, 0
	s_nop 0
	s_nop 0
	v_readlane_b32 s3, v51, 6
	v_readlane_b32 s2, v51, 7
	s_waitcnt lgkmcnt(0)
	v_mfma_f32_32x32x16_f16 v[32:47], v[20:23], v[24:27], v[32:47]
	s_nop 0
	s_nop 0
	v_readlane_b32 s36, v51, 8
	v_readlane_b32 s35, v51, 9
	v_readlane_b32 s34, v51, 10
	v_readlane_b32 s33, v51, 11
	v_readlane_b32 s31, v51, 12
	v_readlane_b32 s30, v51, 13
	v_readlane_b32 s29, v51, 14
	v_readlane_b32 s28, v51, 15
	v_readlane_b32 s27, v51, 16
	v_readlane_b32 s26, v51, 17
	v_readlane_b32 s25, v51, 18
	v_readlane_b32 s24, v51, 19
	v_readlane_b32 s23, v51, 20
	v_readlane_b32 s42, v51, 21
	v_readlane_b32 s41, v51, 22
	v_readlane_b32 s40, v51, 23
	v_readlane_b32 s39, v51, 24
	v_readlane_b32 s38, v51, 25
	v_readlane_b32 s37, v51, 26
	v_readlane_b32 s21, v51, 27
	v_readlane_b32 s20, v51, 28
	v_readlane_b32 s19, v51, 29
	v_readlane_b32 s18, v51, 30
	v_readlane_b32 s10, v51, 31
	ds_read_b128 v[16:19], v69 offset:7168
	s_nop 0
	global_load_dwordx4 v[56:59], v124, s[56:57]
	global_load_dword v80, v124, s[56:57] offset:24
	global_load_dword v51, v124, s[56:57] offset:-8
	global_load_dword v112, v79, s[48:49]
	s_add_u32 s48, s4, s47
	s_addc_u32 s49, s5, 0
	s_lshl_b32 s46, s46, 8
	s_and_b32 s46, s46, 0xffff00
	s_add_u32 s46, s4, s46
	s_addc_u32 s47, s5, 0
	s_lshl_b32 s45, s45, 8
	s_and_b32 s45, s45, 0xffff00
	global_load_dword v110, v79, s[48:49]
	global_load_dword v108, v79, s[46:47]
	s_add_u32 s46, s4, s45
	s_addc_u32 s47, s5, 0
	s_lshl_b32 s44, s44, 8
	s_and_b32 s44, s44, 0xffff00
	s_add_u32 s44, s4, s44
	s_addc_u32 s45, s5, 0
	s_lshl_b32 s43, s43, 8
	s_and_b32 s43, s43, 0xffff00
	global_load_dword v106, v79, s[46:47]
	global_load_dword v104, v79, s[44:45]
	s_add_u32 s44, s4, s43
	s_addc_u32 s45, s5, 0
	s_lshl_b32 s3, s3, 8
	s_and_b32 s3, s3, 0xffff00
	global_load_dword v102, v79, s[44:45]
	s_add_u32 s44, s4, s3
	s_addc_u32 s45, s5, 0
	s_lshl_b32 s2, s2, 8
	s_and_b32 s2, s2, 0xffff00
	s_add_u32 s2, s4, s2
	global_load_dword v100, v79, s[44:45]
	s_addc_u32 s3, s5, 0
	global_load_dword v114, v79, s[2:3]
	s_lshl_b32 s2, s36, 8
	s_and_b32 s2, s2, 0xffff00
	s_add_u32 s2, s4, s2
	s_addc_u32 s3, s5, 0
	global_load_dword v113, v79, s[2:3]
	s_lshl_b32 s2, s35, 8
	s_and_b32 s2, s2, 0xffff00
	s_add_u32 s2, s4, s2
	s_addc_u32 s3, s5, 0
	global_load_dword v111, v79, s[2:3]
	s_lshl_b32 s2, s34, 8
	s_and_b32 s2, s2, 0xffff00
	s_add_u32 s2, s4, s2
	s_addc_u32 s3, s5, 0
	global_load_dword v109, v79, s[2:3]
	s_lshl_b32 s2, s33, 8
	s_and_b32 s2, s2, 0xffff00
	s_add_u32 s2, s4, s2
	s_addc_u32 s3, s5, 0
	global_load_dword v107, v79, s[2:3]
	s_lshl_b32 s2, s31, 8
	s_and_b32 s2, s2, 0xffff00
	s_add_u32 s2, s4, s2
	s_addc_u32 s3, s5, 0
	global_load_dword v105, v79, s[2:3]
	s_lshl_b32 s2, s30, 8
	s_and_b32 s2, s2, 0xffff00
	s_add_u32 s2, s4, s2
	s_addc_u32 s3, s5, 0
	global_load_dword v103, v79, s[2:3]
	s_lshl_b32 s2, s29, 8
	s_and_b32 s2, s2, 0xffff00
	s_add_u32 s2, s4, s2
	s_addc_u32 s3, s5, 0
	global_load_dword v101, v79, s[2:3]
	s_lshl_b32 s2, s28, 8
	s_and_b32 s2, s2, 0xffff00
	s_add_u32 s2, s4, s2
	s_addc_u32 s3, s5, 0
	global_load_dword v98, v79, s[2:3]
	s_lshl_b32 s2, s27, 8
	s_and_b32 s2, s2, 0xffff00
	s_add_u32 s2, s4, s2
	s_addc_u32 s3, s5, 0
	global_load_dword v97, v79, s[2:3]
	s_lshl_b32 s2, s26, 8
	s_and_b32 s2, s2, 0xffff00
	s_add_u32 s2, s4, s2
	s_addc_u32 s3, s5, 0
	global_load_dword v96, v79, s[2:3]
	s_lshl_b32 s2, s25, 8
	s_and_b32 s2, s2, 0xffff00
	s_add_u32 s2, s4, s2
	s_addc_u32 s3, s5, 0
	global_load_dword v94, v79, s[2:3]
	s_lshl_b32 s2, s24, 8
	s_and_b32 s2, s2, 0xffff00
	s_add_u32 s2, s4, s2
	s_addc_u32 s3, s5, 0
	global_load_dword v91, v79, s[2:3]
	s_lshl_b32 s2, s23, 8
	s_and_b32 s2, s2, 0xffff00
	s_add_u32 s2, s4, s2
	s_addc_u32 s3, s5, 0
	global_load_dword v93, v79, s[2:3]
	s_lshl_b32 s2, s42, 8
	s_and_b32 s2, s2, 0xffff00
	s_add_u32 s2, s4, s2
	s_addc_u32 s3, s5, 0
	global_load_dword v90, v79, s[2:3]
	s_lshl_b32 s2, s41, 8
	s_and_b32 s2, s2, 0xffff00
	s_add_u32 s2, s4, s2
	s_addc_u32 s3, s5, 0
	global_load_dword v88, v79, s[2:3]
	s_lshl_b32 s2, s40, 8
	s_and_b32 s2, s2, 0xffff00
	s_add_u32 s2, s4, s2
	s_addc_u32 s3, s5, 0
	global_load_dword v86, v79, s[2:3]
	s_lshl_b32 s2, s39, 8
	s_and_b32 s2, s2, 0xffff00
	s_nop 0
	s_nop 0
	s_add_u32 s2, s4, s2
	s_waitcnt lgkmcnt(0)
	v_mfma_f32_32x32x16_f16 v[32:47], v[16:19], v[82:85], v[32:47]
	v_exp_f32_e32 v0, v0
	v_exp_f32_e32 v1, v1
	s_addc_u32 s3, s5, 0
	global_load_dword v85, v79, s[2:3]
	s_lshl_b32 s2, s38, 8
	s_and_b32 s2, s2, 0xffff00
	s_nop 0
	s_nop 0
	s_add_u32 s2, s4, s2
	v_exp_f32_e32 v6, v6
	v_exp_f32_e32 v7, v7
	s_addc_u32 s3, s5, 0
	global_load_dword v83, v79, s[2:3]
	s_lshl_b32 s2, s37, 8
	v_pk_add_f32 v[0:1], v[0:1], 1.0 op_sel_hi:[1,0]
	s_and_b32 s2, s2, 0xffff00
	s_nop 0
	s_nop 0
	v_min_f32 v16, 0x42fc0000, v4
	v_min_f32 v17, 0x42fc0000, v5
	v_log_f32_e32 v4, v0
	v_log_f32_e32 v5, v1
	v_exp_f32_e32 v0, v16
	v_exp_f32_e32 v1, v17
	s_add_u32 s2, s4, s2
	v_exp_f32_e32 v2, v2
	v_exp_f32_e32 v3, v3
	s_addc_u32 s3, s5, 0
	global_load_dword v92, v79, s[2:3]
	s_lshl_b32 s2, s21, 8
	v_pk_add_f32 v[6:7], v[6:7], 1.0 op_sel_hi:[1,0]
	s_and_b32 s2, s2, 0xffff00
	v_log_f32_e32 v6, v6
	v_log_f32_e32 v7, v7
	s_add_u32 s2, s4, s2
	v_pk_add_f32 v[0:1], v[0:1], 1.0 op_sel_hi:[1,0]
	s_addc_u32 s3, s5, 0
	global_load_dword v89, v79, s[2:3]
	s_lshl_b32 s2, s20, 8
	v_pk_add_f32 v[2:3], v[2:3], 1.0 op_sel_hi:[1,0]
	v_log_f32_e32 v0, v0
	v_log_f32_e32 v1, v1
	s_and_b32 s2, s2, 0xffff00
	v_min_f32 v18, 0x42fc0000, v8
	v_min_f32 v19, 0x42fc0000, v9
	v_log_f32_e32 v8, v2
	v_log_f32_e32 v9, v3
	s_add_u32 s2, s4, s2
	v_pk_mul_f32 v[2:3], v[48:49], v[6:7] op_sel:[1,0]
	v_exp_f32_e32 v6, v18
	v_exp_f32_e32 v7, v19
	s_addc_u32 s3, s5, 0
	s_lshl_b32 s19, s19, 8
	s_and_b32 s19, s19, 0xffff00
	v_pk_mul_f32 v[0:1], v[48:49], v[0:1] op_sel:[1,0]
	s_add_u32 s20, s4, s19
	s_nop 0
	s_nop 0
	v_cvt_pk_f16_f32 v3, v2, v3
	v_cvt_pk_f16_f32 v2, v0, v1
	v_pk_mul_f32 v[0:1], v[48:49], v[8:9] op_sel:[1,0]
	v_pk_mul_f32 v[4:5], v[48:49], v[4:5] op_sel:[1,0]
	s_addc_u32 s21, s5, 0
	s_lshl_b32 s18, s18, 8
	s_nop 0
	s_nop 0
	s_nop 0
	s_nop 0
	v_cvt_pk_f16_f32 v1, v0, v1
	v_cvt_pk_f16_f32 v0, v4, v5
	v_pk_add_f32 v[4:5], v[6:7], 1.0 op_sel_hi:[1,0]
	v_exp_f32_e32 v6, v10
	v_exp_f32_e32 v7, v11
	v_exp_f32_e32 v8, v12
	v_exp_f32_e32 v9, v13
	v_exp_f32_e32 v10, v14
	v_exp_f32_e32 v11, v15
	s_and_b32 s18, s18, 0xffff00
	s_add_u32 s18, s4, s18
	s_addc_u32 s19, s5, 0
	s_lshl_b32 s10, s10, 8
	s_and_b32 s10, s10, 0xffff00
	v_pk_add_f32 v[8:9], v[8:9], 1.0 op_sel_hi:[1,0]
	v_pk_add_f32 v[10:11], v[10:11], 1.0 op_sel_hi:[1,0]
	s_add_u32 s24, s4, s10
	v_pk_add_f32 v[6:7], v[6:7], 1.0 op_sel_hi:[1,0]
	v_log_f32_e32 v8, v8
	v_log_f32_e32 v9, v9
	v_log_f32_e32 v10, v10
	v_log_f32_e32 v11, v11
	s_addc_u32 s25, s5, 0
	global_load_dword v87, v79, s[2:3]
	global_load_dword v84, v79, s[20:21]
	global_load_dword v82, v79, s[18:19]
	global_load_dword v81, v79, s[24:25]
	ds_read_b128 v[12:15], v71
	v_log_f32_e32 v6, v6
	v_log_f32_e32 v7, v7
	v_log_f32_e32 v4, v4
	v_log_f32_e32 v5, v5
	v_pk_mul_f32 v[8:9], v[48:49], v[8:9] op_sel:[1,0]
	v_pk_mul_f32 v[10:11], v[48:49], v[10:11] op_sel:[1,0]
	v_cvt_pk_f16_f32 v118, v8, v9
	v_cvt_pk_f16_f32 v119, v10, v11
	v_pk_mul_f32 v[10:11], v[48:49], v[6:7] op_sel:[1,0]
	ds_read_b128 v[6:9], v71 offset:1024
	s_waitcnt lgkmcnt(1)
	v_mfma_f32_32x32x16_f16 v[16:31], v[0:3], v[12:15], 0
	s_nop 0
	s_nop 0
	v_mul_f32_e64 v4, v49, v4
	v_mul_f32_e64 v5, v49, v5
	v_exp_f32_e32 v32, v32
	v_exp_f32_e32 v33, v33
	s_nop 0
	s_nop 0
	v_cvt_pk_f16_f32 v117, v10, v11
	v_cvt_pk_f16_f32 v116, v4, v5
	v_exp_f32_e32 v36, v36
	v_exp_f32_e32 v37, v37
	v_pk_add_f32 v[32:33], v[32:33], 1.0 op_sel_hi:[1,0]
	s_waitcnt lgkmcnt(0)
	v_mfma_f32_32x32x16_f16 v[16:31], v[116:119], v[6:9], v[16:31]
	v_log_f32_e32 v54, v32
	v_log_f32_e32 v55, v33
	v_pk_add_f32 v[32:33], v[36:37], 1.0 op_sel_hi:[1,0]
	s_nop 0
	s_nop 0
	ds_read_b128 v[4:7], v71 offset:4096
	ds_read_b128 v[120:123], v71 offset:5120
	v_exp_f32_e32 v36, v38
	v_exp_f32_e32 v37, v39
	s_nop 0
	s_nop 0
	s_waitcnt lgkmcnt(1)
	v_mfma_f32_32x32x16_f16 v[0:15], v[0:3], v[4:7], 0
	v_exp_f32_e32 v34, v34
	v_exp_f32_e32 v35, v35
	v_pk_add_f32 v[36:37], v[36:37], 1.0 op_sel_hi:[1,0]
	v_log_f32_e32 v32, v32
	v_log_f32_e32 v33, v33
	v_log_f32_e32 v36, v36
	v_log_f32_e32 v37, v37
	v_pk_add_f32 v[34:35], v[34:35], 1.0 op_sel_hi:[1,0]
	v_pk_mul_f32 v[32:33], v[48:49], v[32:33] op_sel:[1,0]
	v_log_f32_e32 v38, v34
	v_log_f32_e32 v39, v35
	v_pk_mul_f32 v[34:35], v[48:49], v[36:37] op_sel:[1,0]
	v_pk_mul_f32 v[36:37], v[48:49], v[54:55] op_sel:[1,0]
	v_cvt_pk_f16_f32 v35, v34, v35
	v_cvt_pk_f16_f32 v34, v32, v33
	v_pk_mul_f32 v[32:33], v[48:49], v[38:39] op_sel:[1,0]
	s_waitcnt lgkmcnt(0)
	v_mfma_f32_32x32x16_f16 v[0:15], v[116:119], v[120:123], v[0:15]
	v_cvt_pk_f16_f32 v33, v32, v33
	v_cvt_pk_f16_f32 v32, v36, v37
	ds_read_b128 v[36:39], v71 offset:2048
	ds_read_b128 v[116:119], v71 offset:3072
	s_nop 0
	s_nop 0
	v_min_f32 v55, 0x42fc0000, v44
	v_min_f32 v115, 0x42fc0000, v45
	s_waitcnt lgkmcnt(1)
	v_mfma_f32_32x32x16_f16 v[16:31], v[32:35], v[36:39], v[16:31]
	ds_read_b128 v[36:39], v71 offset:6144
	v_exp_f32_e32 v44, v40
	v_exp_f32_e32 v45, v41
	v_min_f32 v52, 0x42fc0000, v42
	v_min_f32 v54, 0x42fc0000, v43
	ds_read_b128 v[40:43], v71 offset:7168
	s_nop 0
	s_waitcnt lgkmcnt(1)
	v_mfma_f32_32x32x16_f16 v[0:15], v[32:35], v[36:39], v[0:15]
	v_add_f32_e64 v34, v44, 1.0
	v_add_f32_e64 v35, v45, 1.0
	s_nop 0
	v_exp_f32_e32 v32, v55
	v_exp_f32_e32 v33, v115
	v_log_f32_e32 v36, v34
	v_log_f32_e32 v37, v35
	v_exp_f32_e32 v34, v46
	v_exp_f32_e32 v35, v47
	v_exp_f32_e32 v38, v52
	v_exp_f32_e32 v39, v54
	v_pk_add_f32 v[32:33], v[32:33], 1.0 op_sel_hi:[1,0]
	v_pk_add_f32 v[34:35], v[34:35], 1.0 op_sel_hi:[1,0]
	v_log_f32_e32 v32, v32
	v_log_f32_e32 v33, v33
	v_log_f32_e32 v34, v34
	v_log_f32_e32 v35, v35
	v_pk_add_f32 v[38:39], v[38:39], 1.0 op_sel_hi:[1,0]
	v_pk_mul_f32 v[32:33], v[48:49], v[32:33] op_sel:[1,0]
	v_log_f32_e32 v38, v38
	v_log_f32_e32 v39, v39
	v_pk_mul_f32 v[34:35], v[48:49], v[34:35] op_sel:[1,0]
	v_pk_mul_f32 v[36:37], v[48:49], v[36:37] op_sel:[1,0]
	v_cvt_pk_f16_f32 v35, v34, v35
	v_cvt_pk_f16_f32 v34, v32, v33
	v_pk_mul_f32 v[32:33], v[48:49], v[38:39] op_sel:[1,0]
	v_mov_b32_e32 v54, v53
	v_cvt_pk_f16_f32 v33, v32, v33
	v_cvt_pk_f16_f32 v32, v36, v37
	v_cvt_f16_f32_e32 v36, v49
	v_mov_b32_e32 v55, v53
	v_mfma_f32_32x32x16_f16 v[16:31], v[32:35], v[116:119], v[16:31]
	v_cmp_ne_u32_sdwa s[20:21], v95, v50 src0_sel:DWORD src1_sel:WORD_1
	v_cmp_ne_u32_sdwa s[18:19], v99, v50 src0_sel:WORD_1 src1_sel:WORD_1
	s_bitcmp1_b32 s20, 0
	v_cmp_lt_i32_e64 s[2:3], s13, v64
	s_cselect_b64 s[20:21], -1, 0
	s_bitcmp0_b32 s18, 0
	s_waitcnt lgkmcnt(0)
	v_mfma_f32_32x32x16_f16 v[0:15], v[32:35], v[40:43], v[0:15]
	v_cndmask_b32_e64 v32, 0, v36, s[0:1]
	v_pack_b32_f16 v52, v32, 0
	ds_read_b128 v[32:35], v72
	ds_read_b128 v[36:39], v72 offset:1024
	s_waitcnt vmcnt(0)
	s_waitcnt vmcnt(0)
	s_waitcnt lgkmcnt(1)
	v_mfma_f32_32x32x16_f16 v[16:31], v[52:55], v[32:35], v[16:31]
	v_mov_b64_e32 v[32:33], 0
	s_nop 0
	s_waitcnt lgkmcnt(0)
	v_mfma_f32_32x32x16_f16 v[0:15], v[52:55], v[36:39], v[0:15]
	s_nop 11
	v_permlane32_swap_b32_e32 v16, v0
	v_permlane32_swap_b32_e32 v17, v1
	v_permlane32_swap_b32_e32 v18, v2
	v_permlane32_swap_b32_e32 v19, v3
	v_permlane32_swap_b32_e32 v20, v4
	v_permlane32_swap_b32_e32 v21, v5
	v_permlane32_swap_b32_e32 v22, v6
	v_permlane32_swap_b32_e32 v23, v7
	v_permlane32_swap_b32_e32 v24, v8
	v_permlane32_swap_b32_e32 v25, v9
	v_permlane32_swap_b32_e32 v26, v10
	v_permlane32_swap_b32_e32 v27, v11
	v_permlane32_swap_b32_e32 v28, v12
	v_permlane32_swap_b32_e32 v29, v13
	v_permlane32_swap_b32_e32 v30, v14
	v_permlane32_swap_b32_e32 v31, v15
	v_fma_mix_f32 v32, v16, v112, v32 op_sel:[0,1,0] op_sel_hi:[0,1,0]
	v_fma_mix_f32 v33, v16, v112, v33 op_sel_hi:[0,1,0]
	s_cbranch_scc1 .LBB4_13
	v_readlane_b32 s10, v50, 0
	s_bfe_u32 s19, s10, 0x80008
	v_lshl_or_b32 v16, s19, 7, v73
	ds_read_u16 v16, v16
	s_bfe_u32 s10, s10, 0x100010
	s_lshl_b32 s10, s10, 8
	s_add_u32 s58, s60, s10
	s_addc_u32 s59, s61, 0
	s_cmp_lg_u64 s[20:21], 0
	s_cselect_b32 s58, s58, s62
	s_cselect_b32 s59, s59, s63
	s_nop 0
	s_waitcnt lgkmcnt(0)
	v_fma_mix_f32 v16, v16, v33, v32 op_sel_hi:[1,0,0]
	s_nop 0
	s_mov_b64 s[20:21], -1
	v_mov_b64_e32 v[32:33], 0
	s_nop 0
	global_store_dword v79, v16, s[58:59] sc1
.LBB4_13:
	s_bitcmp0_b32 s18, 1
	v_fma_mix_f32 v32, v17, v110, v32 op_sel:[0,1,0] op_sel_hi:[0,1,0]
	v_fma_mix_f32 v33, v17, v110, v33 op_sel_hi:[0,1,0]
	s_cbranch_scc1 .LBB4_15
	v_readlane_b32 s10, v50, 1
	s_bfe_u32 s19, s10, 0x80008
	v_lshl_or_b32 v16, s19, 7, v73
	ds_read_u16 v34, v16
	s_bfe_u32 s10, s10, 0x100010
	s_lshl_b32 s10, s10, 8
	s_add_u32 s58, s60, s10
	s_addc_u32 s59, s61, 0
	s_cmp_lg_u64 s[20:21], 0
	s_cselect_b32 s58, s58, s62
	s_cselect_b32 s59, s59, s63
	s_nop 0
	s_waitcnt lgkmcnt(0)
	v_fma_mix_f32 v32, v34, v33, v32 op_sel_hi:[1,0,0]
	s_nop 0
	global_store_dword v79, v32, s[58:59] sc1
	s_mov_b64 s[20:21], -1
	v_mov_b64_e32 v[32:33], 0
	s_nop 0
.LBB4_15:
	s_bitcmp0_b32 s18, 2
	v_fma_mix_f32 v32, v18, v108, v32 op_sel:[0,1,0] op_sel_hi:[0,1,0]
	v_fma_mix_f32 v33, v18, v108, v33 op_sel_hi:[0,1,0]
	s_cbranch_scc1 .LBB4_17
	v_readlane_b32 s10, v50, 2
	s_bfe_u32 s19, s10, 0x80008
	v_lshl_or_b32 v16, s19, 7, v73
	ds_read_u16 v18, v16
	s_bfe_u32 s10, s10, 0x100010
	s_lshl_b32 s10, s10, 8
	s_add_u32 s58, s60, s10
	s_addc_u32 s59, s61, 0
	s_cmp_lg_u64 s[20:21], 0
	s_cselect_b32 s58, s58, s62
	s_cselect_b32 s59, s59, s63
	s_nop 0
	s_waitcnt lgkmcnt(0)
	v_fma_mix_f32 v18, v18, v33, v32 op_sel_hi:[1,0,0]
	s_nop 0
	s_mov_b64 s[20:21], -1
	v_mov_b64_e32 v[32:33], 0
	s_nop 0
	global_store_dword v79, v18, s[58:59] sc1
.LBB4_17:
	s_bitcmp0_b32 s18, 3
	v_fma_mix_f32 v32, v19, v106, v32 op_sel:[0,1,0] op_sel_hi:[0,1,0]
	v_fma_mix_f32 v33, v19, v106, v33 op_sel_hi:[0,1,0]
	s_cbranch_scc1 .LBB4_19
	v_readlane_b32 s10, v50, 3
	s_bfe_u32 s19, s10, 0x80008
	v_lshl_or_b32 v16, s19, 7, v73
	ds_read_u16 v18, v16
	s_bfe_u32 s10, s10, 0x100010
	s_lshl_b32 s10, s10, 8
	s_add_u32 s58, s60, s10
	s_addc_u32 s59, s61, 0
	s_cmp_lg_u64 s[20:21], 0
	s_cselect_b32 s58, s58, s62
	s_cselect_b32 s59, s59, s63
	s_nop 0
	s_waitcnt lgkmcnt(0)
	v_fma_mix_f32 v18, v18, v33, v32 op_sel_hi:[1,0,0]
	s_nop 0
	s_mov_b64 s[20:21], -1
	v_mov_b64_e32 v[32:33], 0
	s_nop 0
	global_store_dword v79, v18, s[58:59] sc1
.LBB4_19:
	s_bitcmp0_b32 s18, 4
	v_fma_mix_f32 v32, v0, v104, v32 op_sel:[0,1,0] op_sel_hi:[0,1,0]
	v_fma_mix_f32 v33, v0, v104, v33 op_sel_hi:[0,1,0]
	s_cbranch_scc1 .LBB4_21
	v_readlane_b32 s10, v50, 4
	s_bfe_u32 s19, s10, 0x80008
	v_lshl_or_b32 v0, s19, 7, v73
	ds_read_u16 v0, v0
	s_bfe_u32 s10, s10, 0x100010
	s_lshl_b32 s10, s10, 8
	s_add_u32 s58, s60, s10
	s_addc_u32 s59, s61, 0
	s_cmp_lg_u64 s[20:21], 0
	s_cselect_b32 s58, s58, s62
	s_cselect_b32 s59, s59, s63
	s_nop 0
	s_waitcnt lgkmcnt(0)
	v_fma_mix_f32 v0, v0, v33, v32 op_sel_hi:[1,0,0]
	s_nop 0
	s_mov_b64 s[20:21], -1
	v_mov_b64_e32 v[32:33], 0
	s_nop 0
	global_store_dword v79, v0, s[58:59] sc1
.LBB4_21:
	s_bitcmp0_b32 s18, 5
	v_fma_mix_f32 v32, v1, v102, v32 op_sel:[0,1,0] op_sel_hi:[0,1,0]
	v_fma_mix_f32 v33, v1, v102, v33 op_sel_hi:[0,1,0]
	s_cbranch_scc1 .LBB4_23
	v_readlane_b32 s10, v50, 5
	s_bfe_u32 s19, s10, 0x80008
	v_lshl_or_b32 v0, s19, 7, v73
	ds_read_u16 v16, v0
	s_bfe_u32 s10, s10, 0x100010
	s_lshl_b32 s10, s10, 8
	s_add_u32 s58, s60, s10
	s_addc_u32 s59, s61, 0
	s_cmp_lg_u64 s[20:21], 0
	s_cselect_b32 s58, s58, s62
	s_cselect_b32 s59, s59, s63
	s_nop 0
	s_waitcnt lgkmcnt(0)
	v_fma_mix_f32 v16, v16, v33, v32 op_sel_hi:[1,0,0]
	s_nop 0
	s_mov_b64 s[20:21], -1
	v_mov_b64_e32 v[32:33], 0
	s_nop 0
	global_store_dword v79, v16, s[58:59] sc1
.LBB4_23:
	s_bitcmp0_b32 s18, 6
	v_fma_mix_f32 v32, v2, v100, v32 op_sel:[0,1,0] op_sel_hi:[0,1,0]
	v_fma_mix_f32 v33, v2, v100, v33 op_sel_hi:[0,1,0]
	s_cbranch_scc1 .LBB4_25
	v_readlane_b32 s10, v50, 6
	s_bfe_u32 s19, s10, 0x80008
	v_lshl_or_b32 v0, s19, 7, v73
	ds_read_u16 v2, v0
	s_bfe_u32 s10, s10, 0x100010
	s_lshl_b32 s10, s10, 8
	s_add_u32 s58, s60, s10
	s_addc_u32 s59, s61, 0
	s_cmp_lg_u64 s[20:21], 0
	s_cselect_b32 s58, s58, s62
	s_cselect_b32 s59, s59, s63
	s_nop 0
	s_waitcnt lgkmcnt(0)
	v_fma_mix_f32 v2, v2, v33, v32 op_sel_hi:[1,0,0]
	s_nop 0
	s_mov_b64 s[20:21], -1
	v_mov_b64_e32 v[32:33], 0
	s_nop 0
	global_store_dword v79, v2, s[58:59] sc1
.LBB4_25:
	s_bitcmp0_b32 s18, 7
	v_fma_mix_f32 v32, v3, v114, v32 op_sel:[0,1,0] op_sel_hi:[0,1,0]
	v_fma_mix_f32 v33, v3, v114, v33 op_sel_hi:[0,1,0]
	s_cbranch_scc1 .LBB4_27
	v_readlane_b32 s10, v50, 7
	s_bfe_u32 s19, s10, 0x80008
	v_lshl_or_b32 v0, s19, 7, v73
	ds_read_u16 v2, v0
	s_bfe_u32 s10, s10, 0x100010
	s_lshl_b32 s10, s10, 8
	s_add_u32 s58, s60, s10
	s_addc_u32 s59, s61, 0
	s_cmp_lg_u64 s[20:21], 0
	s_cselect_b32 s58, s58, s62
	s_cselect_b32 s59, s59, s63
	s_nop 0
	s_waitcnt lgkmcnt(0)
	v_fma_mix_f32 v2, v2, v33, v32 op_sel_hi:[1,0,0]
	s_nop 0
	s_mov_b64 s[20:21], -1
	v_mov_b64_e32 v[32:33], 0
	s_nop 0
	global_store_dword v79, v2, s[58:59] sc1
.LBB4_27:
	s_bitcmp0_b32 s18, 8
	v_fma_mix_f32 v32, v20, v113, v32 op_sel:[0,1,0] op_sel_hi:[0,1,0]
	v_fma_mix_f32 v33, v20, v113, v33 op_sel_hi:[0,1,0]
	s_cbranch_scc1 .LBB4_29
	v_readlane_b32 s10, v50, 8
	s_bfe_u32 s19, s10, 0x80008
	v_lshl_or_b32 v0, s19, 7, v73
	ds_read_u16 v2, v0
	s_bfe_u32 s10, s10, 0x100010
	s_lshl_b32 s10, s10, 8
	s_add_u32 s58, s60, s10
	s_addc_u32 s59, s61, 0
	s_cmp_lg_u64 s[20:21], 0
	s_cselect_b32 s58, s58, s62
	s_cselect_b32 s59, s59, s63
	s_nop 0
	s_waitcnt lgkmcnt(0)
	v_fma_mix_f32 v2, v2, v33, v32 op_sel_hi:[1,0,0]
	s_nop 0
	s_mov_b64 s[20:21], -1
	v_mov_b64_e32 v[32:33], 0
	s_nop 0
	global_store_dword v79, v2, s[58:59] sc1
.LBB4_29:
	s_bitcmp0_b32 s18, 9
	v_fma_mix_f32 v32, v21, v111, v32 op_sel:[0,1,0] op_sel_hi:[0,1,0]
	v_fma_mix_f32 v33, v21, v111, v33 op_sel_hi:[0,1,0]
	s_cbranch_scc1 .LBB4_31
	v_readlane_b32 s10, v50, 9
	s_bfe_u32 s19, s10, 0x80008
	v_lshl_or_b32 v0, s19, 7, v73
	ds_read_u16 v2, v0
	s_bfe_u32 s10, s10, 0x100010
	s_lshl_b32 s10, s10, 8
	s_add_u32 s58, s60, s10
	s_addc_u32 s59, s61, 0
	s_cmp_lg_u64 s[20:21], 0
	s_cselect_b32 s58, s58, s62
	s_cselect_b32 s59, s59, s63
	s_nop 0
	s_waitcnt lgkmcnt(0)
	v_fma_mix_f32 v2, v2, v33, v32 op_sel_hi:[1,0,0]
	s_nop 0
	s_mov_b64 s[20:21], -1
	v_mov_b64_e32 v[32:33], 0
	s_nop 0
	global_store_dword v79, v2, s[58:59] sc1
.LBB4_31:
	s_bitcmp0_b32 s18, 10
	v_fma_mix_f32 v32, v22, v109, v32 op_sel:[0,1,0] op_sel_hi:[0,1,0]
	v_fma_mix_f32 v33, v22, v109, v33 op_sel_hi:[0,1,0]
	s_cbranch_scc1 .LBB4_33
	v_readlane_b32 s10, v50, 10
	s_bfe_u32 s19, s10, 0x80008
	v_lshl_or_b32 v0, s19, 7, v73
	ds_read_u16 v2, v0
	s_bfe_u32 s10, s10, 0x100010
	s_lshl_b32 s10, s10, 8
	s_add_u32 s58, s60, s10
	s_addc_u32 s59, s61, 0
	s_cmp_lg_u64 s[20:21], 0
	s_cselect_b32 s58, s58, s62
	s_cselect_b32 s59, s59, s63
	s_nop 0
	s_waitcnt lgkmcnt(0)
	v_fma_mix_f32 v2, v2, v33, v32 op_sel_hi:[1,0,0]
	s_nop 0
	s_mov_b64 s[20:21], -1
	v_mov_b64_e32 v[32:33], 0
	s_nop 0
	global_store_dword v79, v2, s[58:59] sc1
.LBB4_33:
	s_bitcmp0_b32 s18, 11
	v_fma_mix_f32 v32, v23, v107, v32 op_sel:[0,1,0] op_sel_hi:[0,1,0]
	v_fma_mix_f32 v33, v23, v107, v33 op_sel_hi:[0,1,0]
	s_cbranch_scc1 .LBB4_35
	v_readlane_b32 s10, v50, 11
	s_bfe_u32 s19, s10, 0x80008
	v_lshl_or_b32 v0, s19, 7, v73
	ds_read_u16 v2, v0
	s_bfe_u32 s10, s10, 0x100010
	s_lshl_b32 s10, s10, 8
	s_add_u32 s58, s60, s10
	s_addc_u32 s59, s61, 0
	s_cmp_lg_u64 s[20:21], 0
	s_cselect_b32 s58, s58, s62
	s_cselect_b32 s59, s59, s63
	s_nop 0
	s_waitcnt lgkmcnt(0)
	v_fma_mix_f32 v2, v2, v33, v32 op_sel_hi:[1,0,0]
	s_nop 0
	s_mov_b64 s[20:21], -1
	v_mov_b64_e32 v[32:33], 0
	s_nop 0
	global_store_dword v79, v2, s[58:59] sc1
.LBB4_35:
	s_bitcmp0_b32 s18, 12
	v_fma_mix_f32 v32, v4, v105, v32 op_sel:[0,1,0] op_sel_hi:[0,1,0]
	v_fma_mix_f32 v33, v4, v105, v33 op_sel_hi:[0,1,0]
	s_cbranch_scc1 .LBB4_37
	v_readlane_b32 s10, v50, 12
	s_bfe_u32 s19, s10, 0x80008
	v_lshl_or_b32 v0, s19, 7, v73
	ds_read_u16 v2, v0
	s_bfe_u32 s10, s10, 0x100010
	s_lshl_b32 s10, s10, 8
	s_add_u32 s58, s60, s10
	s_addc_u32 s59, s61, 0
	s_cmp_lg_u64 s[20:21], 0
	s_cselect_b32 s58, s58, s62
	s_cselect_b32 s59, s59, s63
	s_nop 0
	s_waitcnt lgkmcnt(0)
	v_fma_mix_f32 v2, v2, v33, v32 op_sel_hi:[1,0,0]
	s_nop 0
	s_mov_b64 s[20:21], -1
	v_mov_b64_e32 v[32:33], 0
	s_nop 0
	global_store_dword v79, v2, s[58:59] sc1
.LBB4_37:
	s_bitcmp0_b32 s18, 13
	v_fma_mix_f32 v32, v5, v103, v32 op_sel:[0,1,0] op_sel_hi:[0,1,0]
	v_fma_mix_f32 v33, v5, v103, v33 op_sel_hi:[0,1,0]
	s_cbranch_scc1 .LBB4_39
	v_readlane_b32 s10, v50, 13
	s_bfe_u32 s19, s10, 0x80008
	v_lshl_or_b32 v0, s19, 7, v73
	ds_read_u16 v2, v0
	s_bfe_u32 s10, s10, 0x100010
	s_lshl_b32 s10, s10, 8
	s_add_u32 s58, s60, s10
	s_addc_u32 s59, s61, 0
	s_cmp_lg_u64 s[20:21], 0
	s_cselect_b32 s58, s58, s62
	s_cselect_b32 s59, s59, s63
	s_nop 0
	s_waitcnt lgkmcnt(0)
	v_fma_mix_f32 v2, v2, v33, v32 op_sel_hi:[1,0,0]
	s_nop 0
	s_mov_b64 s[20:21], -1
	v_mov_b64_e32 v[32:33], 0
	s_nop 0
	global_store_dword v79, v2, s[58:59] sc1
.LBB4_39:
	s_bitcmp0_b32 s18, 14
	v_fma_mix_f32 v32, v6, v101, v32 op_sel:[0,1,0] op_sel_hi:[0,1,0]
	v_fma_mix_f32 v33, v6, v101, v33 op_sel_hi:[0,1,0]
	s_cbranch_scc1 .LBB4_41
	v_readlane_b32 s10, v50, 14
	s_bfe_u32 s19, s10, 0x80008
	v_lshl_or_b32 v0, s19, 7, v73
	ds_read_u16 v2, v0
	s_bfe_u32 s10, s10, 0x100010
	s_lshl_b32 s10, s10, 8
	s_add_u32 s58, s60, s10
	s_addc_u32 s59, s61, 0
	s_cmp_lg_u64 s[20:21], 0
	s_cselect_b32 s58, s58, s62
	s_cselect_b32 s59, s59, s63
	s_nop 0
	s_waitcnt lgkmcnt(0)
	v_fma_mix_f32 v2, v2, v33, v32 op_sel_hi:[1,0,0]
	s_nop 0
	s_mov_b64 s[20:21], -1
	v_mov_b64_e32 v[32:33], 0
	s_nop 0
	global_store_dword v79, v2, s[58:59] sc1
.LBB4_41:
	s_bitcmp0_b32 s18, 15
	v_fma_mix_f32 v32, v7, v98, v32 op_sel:[0,1,0] op_sel_hi:[0,1,0]
	v_fma_mix_f32 v33, v7, v98, v33 op_sel_hi:[0,1,0]
	s_cbranch_scc1 .LBB4_43
	v_readlane_b32 s10, v50, 15
	s_bfe_u32 s19, s10, 0x80008
	v_lshl_or_b32 v0, s19, 7, v73
	ds_read_u16 v2, v0
	s_bfe_u32 s10, s10, 0x100010
	s_lshl_b32 s10, s10, 8
	s_add_u32 s58, s60, s10
	s_addc_u32 s59, s61, 0
	s_cmp_lg_u64 s[20:21], 0
	s_cselect_b32 s58, s58, s62
	s_cselect_b32 s59, s59, s63
	s_nop 0
	s_waitcnt lgkmcnt(0)
	v_fma_mix_f32 v2, v2, v33, v32 op_sel_hi:[1,0,0]
	s_nop 0
	s_mov_b64 s[20:21], -1
	v_mov_b64_e32 v[32:33], 0
	s_nop 0
	global_store_dword v79, v2, s[58:59] sc1
.LBB4_43:
	s_bitcmp0_b32 s18, 16
	v_fma_mix_f32 v32, v24, v97, v32 op_sel:[0,1,0] op_sel_hi:[0,1,0]
	v_fma_mix_f32 v33, v24, v97, v33 op_sel_hi:[0,1,0]
	s_cbranch_scc1 .LBB4_45
	v_readlane_b32 s10, v50, 16
	s_bfe_u32 s19, s10, 0x80008
	v_lshl_or_b32 v0, s19, 7, v73
	ds_read_u16 v2, v0
	s_bfe_u32 s10, s10, 0x100010
	s_lshl_b32 s10, s10, 8
	s_add_u32 s58, s60, s10
	s_addc_u32 s59, s61, 0
	s_cmp_lg_u64 s[20:21], 0
	s_cselect_b32 s58, s58, s62
	s_cselect_b32 s59, s59, s63
	s_nop 0
	s_waitcnt lgkmcnt(0)
	v_fma_mix_f32 v2, v2, v33, v32 op_sel_hi:[1,0,0]
	s_nop 0
	s_mov_b64 s[20:21], -1
	v_mov_b64_e32 v[32:33], 0
	s_nop 0
	global_store_dword v79, v2, s[58:59] sc1
.LBB4_45:
	s_bitcmp0_b32 s18, 17
	v_fma_mix_f32 v32, v25, v96, v32 op_sel:[0,1,0] op_sel_hi:[0,1,0]
	v_fma_mix_f32 v33, v25, v96, v33 op_sel_hi:[0,1,0]
	s_cbranch_scc1 .LBB4_47
	v_readlane_b32 s10, v50, 17
	s_bfe_u32 s19, s10, 0x80008
	v_lshl_or_b32 v0, s19, 7, v73
	ds_read_u16 v2, v0
	s_bfe_u32 s10, s10, 0x100010
	s_lshl_b32 s10, s10, 8
	s_add_u32 s58, s60, s10
	s_addc_u32 s59, s61, 0
	s_cmp_lg_u64 s[20:21], 0
	s_cselect_b32 s58, s58, s62
	s_cselect_b32 s59, s59, s63
	s_nop 0
	s_waitcnt lgkmcnt(0)
	v_fma_mix_f32 v2, v2, v33, v32 op_sel_hi:[1,0,0]
	s_nop 0
	s_mov_b64 s[20:21], -1
	v_mov_b64_e32 v[32:33], 0
	s_nop 0
	global_store_dword v79, v2, s[58:59] sc1
.LBB4_47:
	s_bitcmp0_b32 s18, 18
	v_fma_mix_f32 v32, v26, v94, v32 op_sel:[0,1,0] op_sel_hi:[0,1,0]
	v_fma_mix_f32 v33, v26, v94, v33 op_sel_hi:[0,1,0]
	s_cbranch_scc1 .LBB4_49
	v_readlane_b32 s10, v50, 18
	s_bfe_u32 s19, s10, 0x80008
	v_lshl_or_b32 v0, s19, 7, v73
	ds_read_u16 v2, v0
	s_bfe_u32 s10, s10, 0x100010
	s_lshl_b32 s10, s10, 8
	s_add_u32 s58, s60, s10
	s_addc_u32 s59, s61, 0
	s_cmp_lg_u64 s[20:21], 0
	s_cselect_b32 s58, s58, s62
	s_cselect_b32 s59, s59, s63
	s_nop 0
	s_waitcnt lgkmcnt(0)
	v_fma_mix_f32 v2, v2, v33, v32 op_sel_hi:[1,0,0]
	s_nop 0
	s_mov_b64 s[20:21], -1
	v_mov_b64_e32 v[32:33], 0
	s_nop 0
	global_store_dword v79, v2, s[58:59] sc1
.LBB4_49:
	s_bitcmp0_b32 s18, 19
	v_fma_mix_f32 v32, v27, v91, v32 op_sel:[0,1,0] op_sel_hi:[0,1,0]
	v_fma_mix_f32 v33, v27, v91, v33 op_sel_hi:[0,1,0]
	s_cbranch_scc1 .LBB4_51
	v_readlane_b32 s10, v50, 19
	s_bfe_u32 s19, s10, 0x80008
	v_lshl_or_b32 v0, s19, 7, v73
	ds_read_u16 v2, v0
	s_bfe_u32 s10, s10, 0x100010
	s_lshl_b32 s10, s10, 8
	s_add_u32 s58, s60, s10
	s_addc_u32 s59, s61, 0
	s_cmp_lg_u64 s[20:21], 0
	s_cselect_b32 s58, s58, s62
	s_cselect_b32 s59, s59, s63
	s_nop 0
	s_waitcnt lgkmcnt(0)
	v_fma_mix_f32 v2, v2, v33, v32 op_sel_hi:[1,0,0]
	s_nop 0
	s_mov_b64 s[20:21], -1
	v_mov_b64_e32 v[32:33], 0
	s_nop 0
	global_store_dword v79, v2, s[58:59] sc1
.LBB4_51:
	s_bitcmp0_b32 s18, 20
	v_fma_mix_f32 v32, v8, v93, v32 op_sel:[0,1,0] op_sel_hi:[0,1,0]
	v_fma_mix_f32 v33, v8, v93, v33 op_sel_hi:[0,1,0]
	s_cbranch_scc1 .LBB4_53
	v_readlane_b32 s10, v50, 20
	s_bfe_u32 s19, s10, 0x80008
	v_lshl_or_b32 v0, s19, 7, v73
	ds_read_u16 v2, v0
	s_bfe_u32 s10, s10, 0x100010
	s_lshl_b32 s10, s10, 8
	s_add_u32 s58, s60, s10
	s_addc_u32 s59, s61, 0
	s_cmp_lg_u64 s[20:21], 0
	s_cselect_b32 s58, s58, s62
	s_cselect_b32 s59, s59, s63
	s_nop 0
	s_waitcnt lgkmcnt(0)
	v_fma_mix_f32 v2, v2, v33, v32 op_sel_hi:[1,0,0]
	s_nop 0
	s_mov_b64 s[20:21], -1
	v_mov_b64_e32 v[32:33], 0
	s_nop 0
	global_store_dword v79, v2, s[58:59] sc1
.LBB4_53:
	s_bitcmp0_b32 s18, 21
	v_fma_mix_f32 v32, v9, v90, v32 op_sel:[0,1,0] op_sel_hi:[0,1,0]
	v_fma_mix_f32 v33, v9, v90, v33 op_sel_hi:[0,1,0]
	s_cbranch_scc1 .LBB4_55
	v_readlane_b32 s10, v50, 21
	s_bfe_u32 s19, s10, 0x80008
	v_lshl_or_b32 v0, s19, 7, v73
	ds_read_u16 v2, v0
	s_bfe_u32 s10, s10, 0x100010
	s_lshl_b32 s10, s10, 8
	s_add_u32 s58, s60, s10
	s_addc_u32 s59, s61, 0
	s_cmp_lg_u64 s[20:21], 0
	s_cselect_b32 s58, s58, s62
	s_cselect_b32 s59, s59, s63
	s_nop 0
	s_waitcnt lgkmcnt(0)
	v_fma_mix_f32 v2, v2, v33, v32 op_sel_hi:[1,0,0]
	s_nop 0
	s_mov_b64 s[20:21], -1
	v_mov_b64_e32 v[32:33], 0
	s_nop 0
	global_store_dword v79, v2, s[58:59] sc1
.LBB4_55:
	s_bitcmp0_b32 s18, 22
	v_fma_mix_f32 v32, v10, v88, v32 op_sel:[0,1,0] op_sel_hi:[0,1,0]
	v_fma_mix_f32 v33, v10, v88, v33 op_sel_hi:[0,1,0]
	s_cbranch_scc1 .LBB4_57
	v_readlane_b32 s10, v50, 22
	s_bfe_u32 s19, s10, 0x80008
	v_lshl_or_b32 v0, s19, 7, v73
	ds_read_u16 v2, v0
	s_bfe_u32 s10, s10, 0x100010
	s_lshl_b32 s10, s10, 8
	s_add_u32 s58, s60, s10
	s_addc_u32 s59, s61, 0
	s_cmp_lg_u64 s[20:21], 0
	s_cselect_b32 s58, s58, s62
	s_cselect_b32 s59, s59, s63
	s_nop 0
	s_waitcnt lgkmcnt(0)
	v_fma_mix_f32 v2, v2, v33, v32 op_sel_hi:[1,0,0]
	s_nop 0
	s_mov_b64 s[20:21], -1
	v_mov_b64_e32 v[32:33], 0
	s_nop 0
	global_store_dword v79, v2, s[58:59] sc1
.LBB4_57:
	s_bitcmp0_b32 s18, 23
	v_fma_mix_f32 v32, v11, v86, v32 op_sel:[0,1,0] op_sel_hi:[0,1,0]
	v_fma_mix_f32 v33, v11, v86, v33 op_sel_hi:[0,1,0]
	s_cbranch_scc1 .LBB4_59
	v_readlane_b32 s10, v50, 23
	s_bfe_u32 s19, s10, 0x80008
	v_lshl_or_b32 v0, s19, 7, v73
	ds_read_u16 v2, v0
	s_bfe_u32 s10, s10, 0x100010
	s_lshl_b32 s10, s10, 8
	s_add_u32 s58, s60, s10
	s_addc_u32 s59, s61, 0
	s_cmp_lg_u64 s[20:21], 0
	s_cselect_b32 s58, s58, s62
	s_cselect_b32 s59, s59, s63
	s_nop 0
	s_waitcnt lgkmcnt(0)
	v_fma_mix_f32 v2, v2, v33, v32 op_sel_hi:[1,0,0]
	s_nop 0
	s_mov_b64 s[20:21], -1
	v_mov_b64_e32 v[32:33], 0
	s_nop 0
	global_store_dword v79, v2, s[58:59] sc1
.LBB4_59:
	s_bitcmp0_b32 s18, 24
	v_fma_mix_f32 v32, v28, v85, v32 op_sel:[0,1,0] op_sel_hi:[0,1,0]
	v_fma_mix_f32 v33, v28, v85, v33 op_sel_hi:[0,1,0]
	s_cbranch_scc1 .LBB4_61
	v_readlane_b32 s10, v50, 24
	s_bfe_u32 s19, s10, 0x80008
	v_lshl_or_b32 v0, s19, 7, v73
	ds_read_u16 v2, v0
	s_bfe_u32 s10, s10, 0x100010
	s_lshl_b32 s10, s10, 8
	s_add_u32 s58, s60, s10
	s_addc_u32 s59, s61, 0
	s_cmp_lg_u64 s[20:21], 0
	s_cselect_b32 s58, s58, s62
	s_cselect_b32 s59, s59, s63
	s_nop 0
	s_waitcnt lgkmcnt(0)
	v_fma_mix_f32 v2, v2, v33, v32 op_sel_hi:[1,0,0]
	s_nop 0
	s_mov_b64 s[20:21], -1
	v_mov_b64_e32 v[32:33], 0
	s_nop 0
	global_store_dword v79, v2, s[58:59] sc1
.LBB4_61:
	s_bitcmp0_b32 s18, 25
	v_fma_mix_f32 v32, v29, v83, v32 op_sel:[0,1,0] op_sel_hi:[0,1,0]
	v_fma_mix_f32 v33, v29, v83, v33 op_sel_hi:[0,1,0]
	s_cbranch_scc1 .LBB4_63
	v_readlane_b32 s10, v50, 25
	s_bfe_u32 s19, s10, 0x80008
	v_lshl_or_b32 v0, s19, 7, v73
	ds_read_u16 v2, v0
	s_bfe_u32 s10, s10, 0x100010
	s_lshl_b32 s10, s10, 8
	s_add_u32 s58, s60, s10
	s_addc_u32 s59, s61, 0
	s_cmp_lg_u64 s[20:21], 0
	s_cselect_b32 s58, s58, s62
	s_cselect_b32 s59, s59, s63
	s_nop 0
	s_waitcnt lgkmcnt(0)
	v_fma_mix_f32 v2, v2, v33, v32 op_sel_hi:[1,0,0]
	s_nop 0
	s_mov_b64 s[20:21], -1
	v_mov_b64_e32 v[32:33], 0
	s_nop 0
	global_store_dword v79, v2, s[58:59] sc1
.LBB4_63:
	s_bitcmp0_b32 s18, 26
	v_fma_mix_f32 v32, v30, v92, v32 op_sel:[0,1,0] op_sel_hi:[0,1,0]
	v_fma_mix_f32 v33, v30, v92, v33 op_sel_hi:[0,1,0]
	s_cbranch_scc1 .LBB4_65
	v_readlane_b32 s10, v50, 26
	s_bfe_u32 s19, s10, 0x80008
	v_lshl_or_b32 v0, s19, 7, v73
	ds_read_u16 v2, v0
	s_bfe_u32 s10, s10, 0x100010
	s_lshl_b32 s10, s10, 8
	s_add_u32 s58, s60, s10
	s_addc_u32 s59, s61, 0
	s_cmp_lg_u64 s[20:21], 0
	s_cselect_b32 s58, s58, s62
	s_cselect_b32 s59, s59, s63
	s_nop 0
	s_waitcnt lgkmcnt(0)
	v_fma_mix_f32 v2, v2, v33, v32 op_sel_hi:[1,0,0]
	s_nop 0
	s_mov_b64 s[20:21], -1
	v_mov_b64_e32 v[32:33], 0
	s_nop 0
	global_store_dword v79, v2, s[58:59] sc1
.LBB4_65:
	s_bitcmp0_b32 s18, 27
	v_fma_mix_f32 v32, v31, v89, v32 op_sel:[0,1,0] op_sel_hi:[0,1,0]
	v_fma_mix_f32 v33, v31, v89, v33 op_sel_hi:[0,1,0]
	s_cbranch_scc1 .LBB4_67
	v_readlane_b32 s10, v50, 27
	s_bfe_u32 s19, s10, 0x80008
	v_lshl_or_b32 v0, s19, 7, v73
	ds_read_u16 v2, v0
	s_bfe_u32 s10, s10, 0x100010
	s_lshl_b32 s10, s10, 8
	s_add_u32 s58, s60, s10
	s_addc_u32 s59, s61, 0
	s_cmp_lg_u64 s[20:21], 0
	s_cselect_b32 s58, s58, s62
	s_cselect_b32 s59, s59, s63
	s_nop 0
	s_waitcnt lgkmcnt(0)
	v_fma_mix_f32 v2, v2, v33, v32 op_sel_hi:[1,0,0]
	s_nop 0
	s_mov_b64 s[20:21], -1
	v_mov_b64_e32 v[32:33], 0
	s_nop 0
	global_store_dword v79, v2, s[58:59] sc1
.LBB4_67:
	s_bitcmp0_b32 s18, 28
	v_fma_mix_f32 v32, v12, v87, v32 op_sel:[0,1,0] op_sel_hi:[0,1,0]
	v_fma_mix_f32 v33, v12, v87, v33 op_sel_hi:[0,1,0]
	s_cbranch_scc1 .LBB4_69
	v_readlane_b32 s10, v50, 28
	s_bfe_u32 s19, s10, 0x80008
	v_lshl_or_b32 v0, s19, 7, v73
	ds_read_u16 v2, v0
	s_bfe_u32 s10, s10, 0x100010
	s_lshl_b32 s10, s10, 8
	s_add_u32 s58, s60, s10
	s_addc_u32 s59, s61, 0
	s_cmp_lg_u64 s[20:21], 0
	s_cselect_b32 s58, s58, s62
	s_cselect_b32 s59, s59, s63
	s_nop 0
	s_waitcnt lgkmcnt(0)
	v_fma_mix_f32 v2, v2, v33, v32 op_sel_hi:[1,0,0]
	s_nop 0
	s_mov_b64 s[20:21], -1
	v_mov_b64_e32 v[32:33], 0
	s_nop 0
	global_store_dword v79, v2, s[58:59] sc1
.LBB4_69:
	s_bitcmp0_b32 s18, 29
	v_fma_mix_f32 v32, v13, v84, v32 op_sel:[0,1,0] op_sel_hi:[0,1,0]
	v_fma_mix_f32 v33, v13, v84, v33 op_sel_hi:[0,1,0]
	s_cbranch_scc1 .LBB4_71
	v_readlane_b32 s10, v50, 29
	s_bfe_u32 s19, s10, 0x80008
	v_lshl_or_b32 v0, s19, 7, v73
	ds_read_u16 v2, v0
	s_bfe_u32 s10, s10, 0x100010
	s_lshl_b32 s10, s10, 8
	s_add_u32 s58, s60, s10
	s_addc_u32 s59, s61, 0
	s_cmp_lg_u64 s[20:21], 0
	s_cselect_b32 s58, s58, s62
	s_cselect_b32 s59, s59, s63
	s_nop 0
	s_waitcnt lgkmcnt(0)
	v_fma_mix_f32 v2, v2, v33, v32 op_sel_hi:[1,0,0]
	s_nop 0
	s_mov_b64 s[20:21], -1
	v_mov_b64_e32 v[32:33], 0
	s_nop 0
	global_store_dword v79, v2, s[58:59] sc1
.LBB4_71:
	s_bitcmp0_b32 s18, 30
	v_fma_mix_f32 v32, v14, v82, v32 op_sel:[0,1,0] op_sel_hi:[0,1,0]
	v_fma_mix_f32 v33, v14, v82, v33 op_sel_hi:[0,1,0]
	s_cbranch_scc1 .LBB4_10
	v_readlane_b32 s10, v50, 30
	s_bfe_u32 s18, s10, 0x80008
	v_lshl_or_b32 v0, s18, 7, v73
	ds_read_u16 v2, v0
	s_bfe_u32 s10, s10, 0x100010
	s_lshl_b32 s10, s10, 8
	s_add_u32 s58, s60, s10
	s_addc_u32 s59, s61, 0
	s_cmp_lg_u64 s[20:21], 0
	s_cselect_b32 s58, s58, s62
	s_cselect_b32 s59, s59, s63
	s_nop 0
	s_waitcnt lgkmcnt(0)
	v_fma_mix_f32 v2, v2, v33, v32 op_sel_hi:[1,0,0]
	s_nop 0
	s_mov_b64 s[20:21], -1
	v_mov_b64_e32 v[32:33], 0
	s_nop 0
	global_store_dword v79, v2, s[58:59] sc1
	s_branch .LBB4_10

	.amdhsa_kernel _Z7k_edge1PK15HIP_vector_typeIfLj4EEPKDv8_DF16_S5_PKfS7_S7_PKDv2_DF16_PfSB_
		.amdhsa_group_segment_fixed_size 31488
		.amdhsa_private_segment_fixed_size 0
		.amdhsa_kernarg_size 328
		.amdhsa_user_sgpr_count 2
		.amdhsa_user_sgpr_dispatch_ptr 0
		.amdhsa_user_sgpr_queue_ptr 0
		.amdhsa_user_sgpr_kernarg_segment_ptr 1
		.amdhsa_user_sgpr_dispatch_id 0
		.amdhsa_user_sgpr_kernarg_preload_length 0
		.amdhsa_user_sgpr_kernarg_preload_offset 0
		.amdhsa_user_sgpr_private_segment_size 0
		.amdhsa_uses_dynamic_stack 0
		.amdhsa_enable_private_segment 0
		.amdhsa_system_sgpr_workgroup_id_x 1
		.amdhsa_system_sgpr_workgroup_id_y 0
		.amdhsa_system_sgpr_workgroup_id_z 0
		.amdhsa_system_sgpr_workgroup_info 0
		.amdhsa_system_vgpr_workitem_id 0
		.amdhsa_next_free_vgpr 125
		.amdhsa_next_free_sgpr 96
		.amdhsa_accum_offset 128
		.amdhsa_reserve_vcc 1
		.amdhsa_float_round_mode_32 0
		.amdhsa_float_round_mode_16_64 0
		.amdhsa_float_denorm_mode_32 3
		.amdhsa_float_denorm_mode_16_64 3
		.amdhsa_dx10_clamp 1
		.amdhsa_ieee_mode 1
		.amdhsa_fp16_overflow 0
		.amdhsa_tg_split 0
		.amdhsa_exception_fp_ieee_invalid_op 0
		.amdhsa_exception_fp_denorm_src 0
		.amdhsa_exception_fp_ieee_div_zero 0
		.amdhsa_exception_fp_ieee_overflow 0
		.amdhsa_exception_fp_ieee_underflow 0
		.amdhsa_exception_fp_ieee_inexact 0
		.amdhsa_exception_int_div_zero 0
	.end_amdhsa_kernel

amdhsa.kernels:
  - .agpr_count:     0
    .args:
      - .actual_access:  read_only
        .address_space:  global
        .offset:         0
        .size:           8
        .value_kind:     global_buffer
      - .actual_access:  write_only
        .address_space:  global
        .offset:         8
        .size:           8
        .value_kind:     global_buffer
      - .offset:         16
        .size:           288
        .value_kind:     by_value
      - .actual_access:  write_only
        .address_space:  global
        .offset:         304
        .size:           8
        .value_kind:     global_buffer
      - .actual_access:  write_only
        .address_space:  global
        .offset:         312
        .size:           8
        .value_kind:     global_buffer
    .group_segment_fixed_size: 1564
    .kernarg_segment_align: 8
    .kernarg_segment_size: 320
    .language:       OpenCL C
    .language_version:
      - 2
      - 0
    .max_flat_workgroup_size: 256
    .name:           _Z8k_bcountPKiPi8PrepArgsPDF16_S3_
    .private_segment_fixed_size: 0
    .sgpr_count:     26
    .sgpr_spill_count: 0
    .symbol:         _Z8k_bcountPKiPi8PrepArgsPDF16_S3_.kd
    .uniform_work_group_size: 1
    .uses_dynamic_stack: false
    .vgpr_count:     26
    .vgpr_spill_count: 0
    .wavefront_size: 64
  - .agpr_count:     0
    .args:
      - .actual_access:  read_only
        .address_space:  global
        .offset:         0
        .size:           8
        .value_kind:     global_buffer
      - .actual_access:  read_only
        .address_space:  global
        .offset:         8
        .size:           8
        .value_kind:     global_buffer
      - .actual_access:  read_only
        .address_space:  global
        .offset:         16
        .size:           8
        .value_kind:     global_buffer
      - .actual_access:  read_only
        .address_space:  global
        .offset:         24
        .size:           8
        .value_kind:     global_buffer
      - .actual_access:  write_only
        .address_space:  global
        .offset:         32
        .size:           8
        .value_kind:     global_buffer
      - .actual_access:  write_only
        .address_space:  global
        .offset:         40
        .size:           8
        .value_kind:     global_buffer
      - .actual_access:  write_only
        .address_space:  global
        .offset:         48
        .size:           8
        .value_kind:     global_buffer
    .group_segment_fixed_size: 19228
    .kernarg_segment_align: 8
    .kernarg_segment_size: 56
    .language:       OpenCL C
    .language_version:
      - 2
      - 0
    .max_flat_workgroup_size: 512
    .name:           _Z10k_bscatterPKfPKiS2_S2_PiP15HIP_vector_typeIfLj2EEPf
    .private_segment_fixed_size: 0
    .sgpr_count:     22
    .sgpr_spill_count: 0
    .symbol:         _Z10k_bscatterPKfPKiS2_S2_PiP15HIP_vector_typeIfLj2EEPf.kd
    .uniform_work_group_size: 1
    .uses_dynamic_stack: false
    .vgpr_count:     67
    .vgpr_spill_count: 0
    .wavefront_size: 64
  - .agpr_count:     0
    .args:
      - .actual_access:  read_only
        .address_space:  global
        .offset:         0
        .size:           8
        .value_kind:     global_buffer
      - .actual_access:  read_only
        .address_space:  global
        .offset:         8
        .size:           8
        .value_kind:     global_buffer
      - .actual_access:  read_only
        .address_space:  global
        .offset:         16
        .size:           8
        .value_kind:     global_buffer
      - .actual_access:  write_only
        .address_space:  global
        .offset:         24
        .size:           8
        .value_kind:     global_buffer
      - .actual_access:  write_only
        .address_space:  global
        .offset:         32
        .size:           8
        .value_kind:     global_buffer
    .group_segment_fixed_size: 1024
    .kernarg_segment_align: 8
    .kernarg_segment_size: 40
    .language:       OpenCL C
    .language_version:
      - 2
      - 0
    .max_flat_workgroup_size: 512
    .name:           _Z7k_bsortPK15HIP_vector_typeIfLj2EEPKiS4_PS_IfLj4EEPi
    .private_segment_fixed_size: 0
    .sgpr_count:     56
    .sgpr_spill_count: 0
    .symbol:         _Z7k_bsortPK15HIP_vector_typeIfLj2EEPKiS4_PS_IfLj4EEPi.kd
    .uniform_work_group_size: 1
    .uses_dynamic_stack: false
    .vgpr_count:     64
    .vgpr_spill_count: 0
    .wavefront_size: 64
  - .agpr_count:     0
    .args:
      - .actual_access:  read_only
        .address_space:  global
        .offset:         0
        .size:           8
        .value_kind:     global_buffer
      - .actual_access:  read_only
        .address_space:  global
        .offset:         8
        .size:           8
        .value_kind:     global_buffer
      - .actual_access:  read_only
        .address_space:  global
        .offset:         16
        .size:           8
        .value_kind:     global_buffer
      - .actual_access:  read_only
        .address_space:  global
        .offset:         24
        .size:           8
        .value_kind:     global_buffer
      - .actual_access:  read_only
        .address_space:  global
        .offset:         32
        .size:           8
        .value_kind:     global_buffer
      - .actual_access:  read_only
        .address_space:  global
        .offset:         40
        .size:           8
        .value_kind:     global_buffer
      - .actual_access:  write_only
        .address_space:  global
        .offset:         48
        .size:           8
        .value_kind:     global_buffer
      - .actual_access:  write_only
        .address_space:  global
        .offset:         56
        .size:           8
        .value_kind:     global_buffer
      - .offset:         64
        .size:           4
        .value_kind:     hidden_block_count_x
      - .offset:         68
        .size:           4
        .value_kind:     hidden_block_count_y
      - .offset:         72
        .size:           4
        .value_kind:     hidden_block_count_z
      - .offset:         76
        .size:           2
        .value_kind:     hidden_group_size_x
      - .offset:         78
        .size:           2
        .value_kind:     hidden_group_size_y
      - .offset:         80
        .size:           2
        .value_kind:     hidden_group_size_z
      - .offset:         82
        .size:           2
        .value_kind:     hidden_remainder_x
      - .offset:         84
        .size:           2
        .value_kind:     hidden_remainder_y
      - .offset:         86
        .size:           2
        .value_kind:     hidden_remainder_z
      - .offset:         104
        .size:           8
        .value_kind:     hidden_global_offset_x
      - .offset:         112
        .size:           8
        .value_kind:     hidden_global_offset_y
      - .offset:         120
        .size:           8
        .value_kind:     hidden_global_offset_z
      - .offset:         128
        .size:           2
        .value_kind:     hidden_grid_dims
    .group_segment_fixed_size: 31488
    .kernarg_segment_align: 8
    .kernarg_segment_size: 320
    .language:       OpenCL C
    .language_version:
      - 2
      - 0
    .max_flat_workgroup_size: 256
    .name:           _Z7k_edge0PK15HIP_vector_typeIfLj4EEPKDv8_DF16_S5_PKfS7_S7_PfS8_
    .private_segment_fixed_size: 0
    .sgpr_count:     59
    .sgpr_spill_count: 0
    .symbol:         _Z7k_edge0PK15HIP_vector_typeIfLj4EEPKDv8_DF16_S5_PKfS7_S7_PfS8_.kd
    .uniform_work_group_size: 1
    .uses_dynamic_stack: false
    .vgpr_count:     96
    .vgpr_spill_count: 0
    .wavefront_size: 64
  - .agpr_count:     0
    .args:
      - .actual_access:  read_only
        .address_space:  global
        .offset:         0
        .size:           8
        .value_kind:     global_buffer
      - .actual_access:  read_only
        .address_space:  global
        .offset:         8
        .size:           8
        .value_kind:     global_buffer
      - .actual_access:  read_only
        .address_space:  global
        .offset:         16
        .size:           8
        .value_kind:     global_buffer
      - .actual_access:  read_only
        .address_space:  global
        .offset:         24
        .size:           8
        .value_kind:     global_buffer
      - .actual_access:  read_only
        .address_space:  global
        .offset:         32
        .size:           8
        .value_kind:     global_buffer
      - .actual_access:  read_only
        .address_space:  global
        .offset:         40
        .size:           8
        .value_kind:     global_buffer
      - .address_space:  global
        .offset:         48
        .size:           8
        .value_kind:     global_buffer
      - .actual_access:  write_only
        .address_space:  global
        .offset:         56
        .size:           8
        .value_kind:     global_buffer
      - .actual_access:  write_only
        .address_space:  global
        .offset:         64
        .size:           8
        .value_kind:     global_buffer
      - .offset:         72
        .size:           4
        .value_kind:     hidden_block_count_x
      - .offset:         76
        .size:           4
        .value_kind:     hidden_block_count_y
      - .offset:         80
        .size:           4
        .value_kind:     hidden_block_count_z
      - .offset:         84
        .size:           2
        .value_kind:     hidden_group_size_x
      - .offset:         86
        .size:           2
        .value_kind:     hidden_group_size_y
      - .offset:         88
        .size:           2
        .value_kind:     hidden_group_size_z
      - .offset:         90
        .size:           2
        .value_kind:     hidden_remainder_x
      - .offset:         92
        .size:           2
        .value_kind:     hidden_remainder_y
      - .offset:         94
        .size:           2
        .value_kind:     hidden_remainder_z
      - .offset:         112
        .size:           8
        .value_kind:     hidden_global_offset_x
      - .offset:         120
        .size:           8
        .value_kind:     hidden_global_offset_y
      - .offset:         128
        .size:           8
        .value_kind:     hidden_global_offset_z
      - .offset:         136
        .size:           2
        .value_kind:     hidden_grid_dims
    .group_segment_fixed_size: 31488
    .kernarg_segment_align: 8
    .kernarg_segment_size: 328
    .language:       OpenCL C
    .language_version:
      - 2
      - 0
    .max_flat_workgroup_size: 256
    .name:           _Z7k_edge1PK15HIP_vector_typeIfLj4EEPKDv8_DF16_S5_PKfS7_S7_PKDv2_DF16_PfSB_
    .private_segment_fixed_size: 0
    .sgpr_count:     56
    .sgpr_spill_count: 0
    .symbol:         _Z7k_edge1PK15HIP_vector_typeIfLj4EEPKDv8_DF16_S5_PKfS7_S7_PKDv2_DF16_PfSB_.kd
    .uniform_work_group_size: 1
    .uses_dynamic_stack: false
    .vgpr_count:     125
    .vgpr_spill_count: 0
    .wavefront_size: 64
  - .agpr_count:     0
    .args:
      - .actual_access:  read_only
        .address_space:  global
        .offset:         0
        .size:           8
        .value_kind:     global_buffer
      - .actual_access:  read_only
        .address_space:  global
        .offset:         8
        .size:           8
        .value_kind:     global_buffer
      - .address_space:  global
        .offset:         16
        .size:           8
        .value_kind:     global_buffer
      - .address_space:  global
        .offset:         24
        .size:           8
        .value_kind:     global_buffer
    .group_segment_fixed_size: 0
    .kernarg_segment_align: 8
    .kernarg_segment_size: 32
    .language:       OpenCL C
    .language_version:
      - 2
      - 0
    .max_flat_workgroup_size: 256
    .name:           _Z6k_poolPKfPKiPfS3_
    .private_segment_fixed_size: 0
    .sgpr_count:     20
    .sgpr_spill_count: 0
    .symbol:         _Z6k_poolPKfPKiPfS3_.kd
    .uniform_work_group_size: 1
    .uses_dynamic_stack: false
    .vgpr_count:     16
    .vgpr_spill_count: 0
    .wavefront_size: 64
  - .agpr_count:     0
    .args:
      - .actual_access:  read_only
        .address_space:  global
        .offset:         0
        .size:           8
        .value_kind:     global_buffer
      - .actual_access:  read_only
        .address_space:  global
        .offset:         8
        .size:           8
        .value_kind:     global_buffer
      - .actual_access:  read_only
        .address_space:  global
        .offset:         16
        .size:           8
        .value_kind:     global_buffer
      - .actual_access:  read_only
        .address_space:  global
        .offset:         24
        .size:           8
        .value_kind:     global_buffer
      - .actual_access:  read_only
        .address_space:  global
        .offset:         32
        .size:           8
        .value_kind:     global_buffer
      - .actual_access:  read_only
        .address_space:  global
        .offset:         40
        .size:           8
        .value_kind:     global_buffer
      - .actual_access:  write_only
        .address_space:  global
        .offset:         48
        .size:           8
        .value_kind:     global_buffer
    .group_segment_fixed_size: 20480
    .kernarg_segment_align: 8
    .kernarg_segment_size: 56
    .language:       OpenCL C
    .language_version:
      - 2
      - 0
    .max_flat_workgroup_size: 64
    .name:           _Z7k_finalPKfS0_S0_S0_S0_S0_Pf
    .private_segment_fixed_size: 0
    .sgpr_count:     42
    .sgpr_spill_count: 0
    .symbol:         _Z7k_finalPKfS0_S0_S0_S0_S0_Pf.kd
    .uniform_work_group_size: 1
    .uses_dynamic_stack: false
    .vgpr_count:     144
    .vgpr_spill_count: 0
    .wavefront_size: 64
  - .agpr_count:     0
    .args:
      - .actual_access:  read_only
        .address_space:  global
        .offset:         0
        .size:           8
        .value_kind:     global_buffer
      - .address_space:  global
        .offset:         8
        .size:           8
        .value_kind:     global_buffer
      - .address_space:  global
        .offset:         16
        .size:           8
        .value_kind:     global_buffer
      - .actual_access:  read_only
        .address_space:  global
        .offset:         24
        .size:           8
        .value_kind:     global_buffer
      - .actual_access:  read_only
        .address_space:  global
        .offset:         32
        .size:           8
        .value_kind:     global_buffer
      - .actual_access:  read_only
        .address_space:  global
        .offset:         40
        .size:           8
        .value_kind:     global_buffer
      - .actual_access:  read_only
        .address_space:  global
        .offset:         48
        .size:           8
        .value_kind:     global_buffer
      - .actual_access:  read_only
        .address_space:  global
        .offset:         56
        .size:           8
        .value_kind:     global_buffer
      - .actual_access:  read_only
        .address_space:  global
        .offset:         64
        .size:           8
        .value_kind:     global_buffer
      - .actual_access:  read_only
        .address_space:  global
        .offset:         72
        .size:           8
        .value_kind:     global_buffer
      - .actual_access:  read_only
        .address_space:  global
        .offset:         80
        .size:           8
        .value_kind:     global_buffer
      - .actual_access:  read_only
        .address_space:  global
        .offset:         88
        .size:           8
        .value_kind:     global_buffer
      - .actual_access:  read_only
        .address_space:  global
        .offset:         96
        .size:           8
        .value_kind:     global_buffer
      - .actual_access:  read_only
        .address_space:  global
        .offset:         104
        .size:           8
        .value_kind:     global_buffer
      - .actual_access:  read_only
        .address_space:  global
        .offset:         112
        .size:           8
        .value_kind:     global_buffer
    .group_segment_fixed_size: 59392
    .kernarg_segment_align: 8
    .kernarg_segment_size: 120
    .language:       OpenCL C
    .language_version:
      - 2
      - 0
    .max_flat_workgroup_size: 256
    .name:           _Z6k_nodeILi0ELi0EEvPfS0_PDv2_DF16_PKiPKfS4_S0_S0_S4_S6_PKDv8_DF16_S6_S9_S6_S9_
    .private_segment_fixed_size: 0
    .sgpr_count:     30
    .sgpr_spill_count: 0
    .symbol:         _Z6k_nodeILi0ELi0EEvPfS0_PDv2_DF16_PKiPKfS4_S0_S0_S4_S6_PKDv8_DF16_S6_S9_S6_S9_.kd
    .uniform_work_group_size: 1
    .uses_dynamic_stack: false
    .vgpr_count:     154
    .vgpr_spill_count: 0
    .wavefront_size: 64
  - .agpr_count:     0
    .args:
      - .actual_access:  read_only
        .address_space:  global
        .offset:         0
        .size:           8
        .value_kind:     global_buffer
      - .address_space:  global
        .offset:         8
        .size:           8
        .value_kind:     global_buffer
      - .address_space:  global
        .offset:         16
        .size:           8
        .value_kind:     global_buffer
      - .actual_access:  read_only
        .address_space:  global
        .offset:         24
        .size:           8
        .value_kind:     global_buffer
      - .actual_access:  read_only
        .address_space:  global
        .offset:         32
        .size:           8
        .value_kind:     global_buffer
      - .actual_access:  read_only
        .address_space:  global
        .offset:         40
        .size:           8
        .value_kind:     global_buffer
      - .actual_access:  read_only
        .address_space:  global
        .offset:         48
        .size:           8
        .value_kind:     global_buffer
      - .actual_access:  read_only
        .address_space:  global
        .offset:         56
        .size:           8
        .value_kind:     global_buffer
      - .actual_access:  read_only
        .address_space:  global
        .offset:         64
        .size:           8
        .value_kind:     global_buffer
      - .actual_access:  read_only
        .address_space:  global
        .offset:         72
        .size:           8
        .value_kind:     global_buffer
      - .actual_access:  read_only
        .address_space:  global
        .offset:         80
        .size:           8
        .value_kind:     global_buffer
      - .actual_access:  read_only
        .address_space:  global
        .offset:         88
        .size:           8
        .value_kind:     global_buffer
      - .actual_access:  read_only
        .address_space:  global
        .offset:         96
        .size:           8
        .value_kind:     global_buffer
      - .actual_access:  read_only
        .address_space:  global
        .offset:         104
        .size:           8
        .value_kind:     global_buffer
      - .actual_access:  read_only
        .address_space:  global
        .offset:         112
        .size:           8
        .value_kind:     global_buffer
    .group_segment_fixed_size: 59392
    .kernarg_segment_align: 8
    .kernarg_segment_size: 120
    .language:       OpenCL C
    .language_version:
      - 2
      - 0
    .max_flat_workgroup_size: 256
    .name:           _Z6k_nodeILi1ELi0EEvPfS0_PDv2_DF16_PKiPKfS4_S0_S0_S4_S6_PKDv8_DF16_S6_S9_S6_S9_
    .private_segment_fixed_size: 0
    .sgpr_count:     30
    .sgpr_spill_count: 0
    .symbol:         _Z6k_nodeILi1ELi0EEvPfS0_PDv2_DF16_PKiPKfS4_S0_S0_S4_S6_PKDv8_DF16_S6_S9_S6_S9_.kd
    .uniform_work_group_size: 1
    .uses_dynamic_stack: false
    .vgpr_count:     220
    .vgpr_spill_count: 0
    .wavefront_size: 64
  - .agpr_count:     0
    .args:
      - .actual_access:  read_only
        .address_space:  global
        .offset:         0
        .size:           8
        .value_kind:     global_buffer
      - .actual_access:  read_only
        .address_space:  global
        .offset:         8
        .size:           8
        .value_kind:     global_buffer
      - .address_space:  global
        .offset:         16
        .size:           8
        .value_kind:     global_buffer
      - .actual_access:  read_only
        .address_space:  global
        .offset:         24
        .size:           8
        .value_kind:     global_buffer
      - .actual_access:  read_only
        .address_space:  global
        .offset:         32
        .size:           8
        .value_kind:     global_buffer
      - .actual_access:  read_only
        .address_space:  global
        .offset:         40
        .size:           8
        .value_kind:     global_buffer
      - .address_space:  global
        .offset:         48
        .size:           8
        .value_kind:     global_buffer
      - .address_space:  global
        .offset:         56
        .size:           8
        .value_kind:     global_buffer
      - .actual_access:  read_only
        .address_space:  global
        .offset:         64
        .size:           8
        .value_kind:     global_buffer
      - .actual_access:  read_only
        .address_space:  global
        .offset:         72
        .size:           8
        .value_kind:     global_buffer
      - .actual_access:  read_only
        .address_space:  global
        .offset:         80
        .size:           8
        .value_kind:     global_buffer
      - .actual_access:  read_only
        .address_space:  global
        .offset:         88
        .size:           8
        .value_kind:     global_buffer
      - .actual_access:  read_only
        .address_space:  global
        .offset:         96
        .size:           8
        .value_kind:     global_buffer
      - .actual_access:  read_only
        .address_space:  global
        .offset:         104
        .size:           8
        .value_kind:     global_buffer
      - .actual_access:  read_only
        .address_space:  global
        .offset:         112
        .size:           8
        .value_kind:     global_buffer
    .group_segment_fixed_size: 59392
    .kernarg_segment_align: 8
    .kernarg_segment_size: 120
    .language:       OpenCL C
    .language_version:
      - 2
      - 0
    .max_flat_workgroup_size: 256
    .name:           _Z6k_nodeILi1ELi1EEvPfS0_PDv2_DF16_PKiPKfS4_S0_S0_S4_S6_PKDv8_DF16_S6_S9_S6_S9_
    .private_segment_fixed_size: 0
    .sgpr_count:     30
    .sgpr_spill_count: 0
    .symbol:         _Z6k_nodeILi1ELi1EEvPfS0_PDv2_DF16_PKiPKfS4_S0_S0_S4_S6_PKDv8_DF16_S6_S9_S6_S9_.kd
    .uniform_work_group_size: 1
    .uses_dynamic_stack: false
    .vgpr_count:     220
    .vgpr_spill_count: 0
    .wavefront_size: 64
